# g2p + one static priority raise for waves 4-7 also through the GLA and dilated-attention phases (phases 2-4)
# speedup vs baseline: 1.0091x; 1.0091x over previous
; #define FA_SBAR() __builtin_amdgcn_sched_barrier(0)
; __device__ __forceinline__ int v_rd_base(int lane) { return ((lane & 3) << 3) | (((lane >> 2) & 3) << 6) | (((lane >> 4) & 1) << 5) | (((lane >> 5) & 1) << 8); }
; __device__ __forceinline__ fa::s16x4 tr_read_dyn(int addr) { fa::s16x4 r; asm volatile("ds_read_b64_tr_b16 %0, %1" : "=&v"(r) : "v"(addr) : "memory"); return r; }
; #define INP(k) ldptr(PTAB, (k))
; __device__ __forceinline__ void gla_g1(LAS unsigned char* lds, const bf16* Z, bf16* ST, float* DEC, const GlaPre pre, const float (&wa)[16], const float ba, int item, int tid) {
;     ...
;     const int rb = v_rd_base(lane); const int vbV = (int)(uintptr_t)(lds + GL_V) + (wid >> 2) * 16384 + rb, vbK = (int)(uintptr_t)(lds + GL_KS) + rb;
; #pragma unroll
;     for (int ks = 0; ks < 4; ++ks) {
;         s16x4 bl = tr_read_dyn(vbV + v_rd_off(wid & 3, ks, 0)), bhh = tr_read_dyn(vbV + v_rd_off(wid & 3, ks, 1));
;         s16x4 al[4], ah[4];
; #pragma unroll
;         for (int kt = 0; kt < 4; ++kt) { al[kt] = tr_read_dyn(vbK + v_rd_off(kt, ks, 0)); ah[kt] = tr_read_dyn(vbK + v_rd_off(kt, ks, 1)); }
;         asm volatile("s_waitcnt lgkmcnt(0)" : "+v"(bl), "+v"(bhh), "+v"(al[0]), "+v"(ah[0]), "+v"(al[1]), "+v"(ah[1]), "+v"(al[2]), "+v"(ah[2]), "+v"(al[3]), "+v"(ah[3]) :: "memory"); FA_SBAR();
; #pragma unroll
;         for (int kt = 0; kt < 4; ++kt) acc[kt] = __builtin_amdgcn_mfma_f32_32x32x16_bf16(GL_PK(al[kt], ah[kt]), GL_PK(bl, bhh), acc[kt], 0, 0, 0);
;     }
; __global__ void __launch_bounds__(NWAVES * 64, 2) fwd_kernel(Args args) {
;     ...
;               for (int it = vcu; it < 1024; it += G) { float wa[16], ba; gla_alpha_load(wa, ba, INP(6) + (size_t)l * 16 * 512, INP(7) + l * 512, (it >> 6) & 3, tid);
;                   const GlaPre cur = gla_blr_load(WSP(WS_ZABC), (size_t)(it >> 8) * SEQ + 64 * (it & 63), tid);
;                   gla_g1(ring, WSP(WS_ZABC), ((bf16*)xo), (float*)(ws + WS_GLADEC), cur, wa, ba, it, tid); } }
.LBB0_913:
	s_or_b64 exec, exec, s[38:39]
	s_lshl_b32 s0, s88, 9
	s_mov_b32 s1, s95
	v_writelane_b32 v255, s0, 31
	v_readlane_b32 s12, v252, 6
	v_readlane_b32 s8, v252, 4
	v_writelane_b32 v255, s1, 32
	v_readlane_b32 s18, v252, 12
	v_readlane_b32 s19, v252, 13
	v_readlane_b32 s0, v252, 32
	v_readlane_b32 s9, v252, 5
	s_mov_b64 s[4:5], s[18:19]
	v_readlane_b32 s1, v252, 33
	s_waitcnt lgkmcnt(0)
	s_barrier
	s_lshl_b32 s50, s88, 13
	s_mov_b32 s51, s95
	v_mbcnt_lo_u32_b32 v0, -1, 0
	v_mbcnt_hi_u32_b32 v0, -1, v0
	s_andn2_b64 vcc, exec, s[0:1]
	v_readlane_b32 s13, v252, 7
	v_readlane_b32 s14, v252, 8
	v_readlane_b32 s15, v252, 9
	v_readlane_b32 s16, v252, 10
	v_readlane_b32 s17, v252, 11
	v_mbcnt_lo_u32_b32 v0, -1, 0
	v_mbcnt_hi_u32_b32 v0, -1, v0
	s_cbranch_vccnz .LBB0_924
	v_readlane_b32 s0, v252, 37
	s_add_u32 s6, s8, 0x15600000
	s_addc_u32 s7, s9, 0
	v_add_u32_e32 v72, s0, v0
	v_readlane_b32 s0, v254, 14
	v_ashrrev_i32_e32 v66, 4, v72
	v_and_b32_e32 v0, 15, v0
	s_add_u32 s10, s8, s0
	v_readlane_b32 s0, v254, 15
	v_readlane_b32 s12, v254, 8
	v_readlane_b32 s14, v254, 12
	v_and_b32_e32 v73, 0x7f, v72
	v_ashrrev_i32_e32 v67, 31, v66
	s_addc_u32 s11, s9, s0
	v_lshlrev_b32_e32 v68, 1, v0
	v_readlane_b32 s13, v254, 9
	v_readlane_b32 s0, v253, 58
	s_mov_b32 s1, s14
	v_readlane_b32 s15, v254, 13
	v_readlane_b32 s98, v252, 37
	s_nop 3
	s_cmpk_lt_u32 s98, 0x100
	s_cbranch_scc1 .Lprio_g1_done
	s_setprio 1
.Lprio_g1_done:
	s_branch .LBB0_916
.LBB0_915:
	s_or_b64 exec, exec, s[14:15]
	s_lshl_b32 s15, s18, 6
	v_and_b32_e32 v2, 0xc0, v39
	v_lshlrev_b32_e32 v3, 1, v70
	s_and_b32 s15, s15, 0xffffc000
	v_and_or_b32 v2, v50, 24, v2
	v_and_b32_e32 v3, 32, v3
	v_and_b32_e32 v4, 0x100, v50
	s_add_i32 s15, s15, 0
	v_or3_b32 v69, v2, v3, v4
	s_add_i32 s15, s15, 0x10000
	s_ashr_i32 s14, s18, 6
	v_add_u32_e32 v71, s15, v69
	s_add_i32 s15, 0, 0x8000
	v_add_u32_e32 v8, s15, v69
	s_lshl_b32 s15, s14, 9
	s_and_b32 s15, s15, 0x600
	s_waitcnt lgkmcnt(0)
	s_barrier
	v_add_u32_e32 v94, 0x800, v71
	v_add_u32_e32 v4, s15, v71
	ds_read_b64_tr_b16 v[2:3], v4
	v_add_u32_e32 v6, s15, v94
	ds_read_b64_tr_b16 v[4:5], v6
	v_readlane_b32 s16, v254, 46
	ds_read_b64_tr_b16 v[6:7], v8
	v_and_b32_e32 v0, 31, v70
	s_nop 0
	v_add_u32_e32 v10, s16, v69
	ds_read_b64_tr_b16 v[8:9], v10
	v_readlane_b32 s16, v254, 47
	s_nop 1
	v_add_u32_e32 v12, s16, v69
	ds_read_b64_tr_b16 v[10:11], v12
	v_readlane_b32 s16, v254, 48
	s_nop 1
	v_add_u32_e32 v14, s16, v69
	ds_read_b64_tr_b16 v[12:13], v14
	v_readlane_b32 s16, v254, 49
	s_nop 1
	v_add_u32_e32 v16, s16, v69
	ds_read_b64_tr_b16 v[14:15], v16
	v_readlane_b32 s16, v254, 50
	s_nop 1
	v_add_u32_e32 v18, s16, v69
	ds_read_b64_tr_b16 v[16:17], v18
	v_readlane_b32 s16, v254, 51
	s_nop 1
	v_add_u32_e32 v18, s16, v69
	ds_read_b64_tr_b16 v[74:75], v18
	v_readlane_b32 s16, v254, 52
	s_nop 1
	v_add_u32_e32 v18, s16, v69
	ds_read_b64_tr_b16 v[76:77], v18
	s_nop 0
	s_waitcnt lgkmcnt(0)
	s_or_b32 s16, s15, 0x1000
	v_mfma_f32_32x32x16_bf16 v[50:65], v[6:9], v[2:5], 0
	v_add_u32_e32 v78, s16, v94
	v_mfma_f32_32x32x16_bf16 v[34:49], v[10:13], v[2:5], 0
	v_mfma_f32_32x32x16_bf16 v[18:33], v[14:17], v[2:5], 0
	v_mfma_f32_32x32x16_bf16 v[2:17], v[74:77], v[2:5], 0
	v_add_u32_e32 v76, s16, v71
	ds_read_b64_tr_b16 v[74:75], v76
	ds_read_b64_tr_b16 v[76:77], v78
	v_readlane_b32 s16, v254, 53
	s_nop 1
	v_add_u32_e32 v80, s16, v69
	ds_read_b64_tr_b16 v[78:79], v80
	v_readlane_b32 s16, v254, 54
	s_nop 1
	v_add_u32_e32 v82, s16, v69
	ds_read_b64_tr_b16 v[80:81], v82
	v_readlane_b32 s16, v254, 55
	s_nop 1
	v_add_u32_e32 v84, s16, v69
	ds_read_b64_tr_b16 v[82:83], v84
	v_readlane_b32 s16, v254, 56
	s_nop 1
	v_add_u32_e32 v86, s16, v69
	ds_read_b64_tr_b16 v[84:85], v86
	v_readlane_b32 s16, v254, 57
	s_nop 1
	v_add_u32_e32 v88, s16, v69
	ds_read_b64_tr_b16 v[86:87], v88
	v_readlane_b32 s16, v254, 58
	s_nop 1
	v_add_u32_e32 v90, s16, v69
	ds_read_b64_tr_b16 v[88:89], v90
	v_readlane_b32 s16, v254, 59
	s_nop 1
	v_add_u32_e32 v92, s16, v69
	ds_read_b64_tr_b16 v[90:91], v92
	v_readlane_b32 s16, v254, 60
	s_nop 1
	v_add_u32_e32 v95, s16, v69
	ds_read_b64_tr_b16 v[92:93], v95
	s_nop 0
	s_waitcnt lgkmcnt(0)
	s_or_b32 s16, s15, 0x2000
	v_mfma_f32_32x32x16_bf16 v[50:65], v[78:81], v[74:77], v[50:65]
	v_add_u32_e32 v78, s16, v94
	v_mfma_f32_32x32x16_bf16 v[34:49], v[82:85], v[74:77], v[34:49]
	v_mfma_f32_32x32x16_bf16 v[18:33], v[86:89], v[74:77], v[18:33]
	v_mfma_f32_32x32x16_bf16 v[2:17], v[90:93], v[74:77], v[2:17]
	v_add_u32_e32 v76, s16, v71
	ds_read_b64_tr_b16 v[74:75], v76
	ds_read_b64_tr_b16 v[76:77], v78
	s_add_i32 s16, 0, 0xa000
	v_add_u32_e32 v80, s16, v69
	ds_read_b64_tr_b16 v[78:79], v80
	v_readlane_b32 s16, v254, 61
	s_nop 1
	v_add_u32_e32 v82, s16, v69
	ds_read_b64_tr_b16 v[80:81], v82
	v_readlane_b32 s16, v254, 62
	s_nop 1
	v_add_u32_e32 v84, s16, v69
	ds_read_b64_tr_b16 v[82:83], v84
	v_readlane_b32 s16, v254, 63
	s_nop 1
	v_add_u32_e32 v86, s16, v69
	ds_read_b64_tr_b16 v[84:85], v86
	v_readlane_b32 s16, v255, 0
	s_nop 1
	v_add_u32_e32 v88, s16, v69
	ds_read_b64_tr_b16 v[86:87], v88
	v_readlane_b32 s16, v255, 1
	s_nop 1
	v_add_u32_e32 v90, s16, v69
	ds_read_b64_tr_b16 v[88:89], v90
	v_readlane_b32 s16, v255, 2
	s_nop 1
	v_add_u32_e32 v92, s16, v69
	ds_read_b64_tr_b16 v[90:91], v92
	v_readlane_b32 s16, v255, 3
	s_nop 1
	v_add_u32_e32 v95, s16, v69
	ds_read_b64_tr_b16 v[92:93], v95
	s_nop 0
	s_waitcnt lgkmcnt(0)
; __device__ __forceinline__ unsigned pk2(float lo, float hi) { return f2bf(lo) | (f2bf(hi) << 16); }
; #define FA_SBAR() __builtin_amdgcn_sched_barrier(0)
; __device__ __forceinline__ fa::s16x4 tr_read_dyn(int addr) { fa::s16x4 r; asm volatile("ds_read_b64_tr_b16 %0, %1" : "=&v"(r) : "v"(addr) : "memory"); return r; }
; __device__ __forceinline__ void gla_g1(LAS unsigned char* lds, const bf16* Z, bf16* ST, float* DEC, const GlaPre pre, const float (&wa)[16], const float ba, int item, int tid) {
;     ...
;     for (int ks = 0; ks < 4; ++ks) {
;         s16x4 bl = tr_read_dyn(vbV + v_rd_off(wid & 3, ks, 0)), bhh = tr_read_dyn(vbV + v_rd_off(wid & 3, ks, 1));
;         s16x4 al[4], ah[4];
; #pragma unroll
;         for (int kt = 0; kt < 4; ++kt) { al[kt] = tr_read_dyn(vbK + v_rd_off(kt, ks, 0)); ah[kt] = tr_read_dyn(vbK + v_rd_off(kt, ks, 1)); }
;         asm volatile("s_waitcnt lgkmcnt(0)" : "+v"(bl), "+v"(bhh), "+v"(al[0]), "+v"(ah[0]), "+v"(al[1]), "+v"(ah[1]), "+v"(al[2]), "+v"(ah[2]), "+v"(al[3]), "+v"(ah[3]) :: "memory"); FA_SBAR();
; #pragma unroll
;         for (int kt = 0; kt < 4; ++kt) acc[kt] = __builtin_amdgcn_mfma_f32_32x32x16_bf16(GL_PK(al[kt], ah[kt]), GL_PK(bl, bhh), acc[kt], 0, 0, 0);
;     }
;     bf16* stp = ST + ((size_t)item * 256 + 32 * wid + r32) * 128 + 4 * hf;
; #pragma unroll
;     for (int kt = 0; kt < 4; ++kt)
; #pragma unroll
;         for (int g = 0; g < 4; ++g) { v2u w; w.x = pk2(acc[kt][4 * g], acc[kt][4 * g + 1]); w.y = pk2(acc[kt][4 * g + 2], acc[kt][4 * g + 3]); *(v2u*)(stp + 32 * kt + 8 * g) = w; }
;     __syncthreads();
	s_or_b32 s15, s15, 0x3000
	v_mfma_f32_32x32x16_bf16 v[50:65], v[78:81], v[74:77], v[50:65]
	v_add_u32_e32 v71, s15, v71
	v_mfma_f32_32x32x16_bf16 v[34:49], v[82:85], v[74:77], v[34:49]
	v_mfma_f32_32x32x16_bf16 v[18:33], v[86:89], v[74:77], v[18:33]
	v_mfma_f32_32x32x16_bf16 v[2:17], v[90:93], v[74:77], v[2:17]
	ds_read_b64_tr_b16 v[74:75], v71
	v_add_u32_e32 v71, s15, v94
	ds_read_b64_tr_b16 v[76:77], v71
	s_add_i32 s15, 0, 0xb000
	v_add_u32_e32 v71, s15, v69
	ds_read_b64_tr_b16 v[78:79], v71
	v_readlane_b32 s15, v255, 4
	s_nop 1
	v_add_u32_e32 v71, s15, v69
	ds_read_b64_tr_b16 v[80:81], v71
	v_readlane_b32 s15, v255, 5
	s_nop 1
	v_add_u32_e32 v71, s15, v69
	ds_read_b64_tr_b16 v[82:83], v71
	v_readlane_b32 s15, v255, 6
	s_nop 1
	v_add_u32_e32 v71, s15, v69
	ds_read_b64_tr_b16 v[84:85], v71
	v_readlane_b32 s15, v255, 7
	s_nop 1
	v_add_u32_e32 v71, s15, v69
	ds_read_b64_tr_b16 v[86:87], v71
	v_readlane_b32 s15, v255, 8
	s_nop 1
	v_add_u32_e32 v71, s15, v69
	ds_read_b64_tr_b16 v[88:89], v71
	v_readlane_b32 s15, v255, 9
	s_nop 1
	v_add_u32_e32 v71, s15, v69
	ds_read_b64_tr_b16 v[90:91], v71
	v_readlane_b32 s15, v255, 10
	s_nop 1
	v_add_u32_e32 v69, s15, v69
	ds_read_b64_tr_b16 v[92:93], v69
	s_nop 0
	s_waitcnt lgkmcnt(0)
	s_nop 0
	v_mfma_f32_32x32x16_bf16 v[50:65], v[78:81], v[74:77], v[50:65]
	s_lshl_b32 s14, s14, 5
	s_ashr_i32 s15, s14, 31
	s_add_u32 s14, s12, s14
	s_addc_u32 s15, s13, s15
	s_add_i32 s1, s1, s78
	v_mfma_f32_32x32x16_bf16 v[34:49], v[82:85], v[74:77], v[34:49]
	v_mfma_f32_32x32x16_bf16 v[18:33], v[86:89], v[74:77], v[18:33]
	v_mfma_f32_32x32x16_bf16 v[2:17], v[90:93], v[74:77], v[2:17]
	v_lshl_add_u64 v[74:75], s[14:15], 0, v[0:1]
	v_lshlrev_b64 v[74:75], 8, v[74:75]
	v_lshrrev_b32_e32 v0, 2, v70
	v_lshl_add_u64 v[74:75], s[4:5], 0, v[74:75]
	v_and_b32_e32 v0, 8, v0
	v_lshl_add_u64 v[70:71], v[74:75], 0, v[0:1]
	v_lshl_add_u64 v[74:75], v[0:1], 1, v[74:75]
	v_bfe_u32 v0, v50, 16, 1
	v_add3_u32 v0, v50, v0, s40
	v_bfe_u32 v50, v51, 16, 1
	v_lshrrev_b32_e32 v0, 16, v0
	v_add3_u32 v50, v51, v50, s40
	v_and_or_b32 v50, v50, s41, v0
	v_bfe_u32 v0, v52, 16, 1
	v_add3_u32 v0, v52, v0, s40
	v_bfe_u32 v51, v53, 16, 1
	v_lshrrev_b32_e32 v0, 16, v0
	v_add3_u32 v51, v53, v51, s40
	v_and_or_b32 v51, v51, s41, v0
	v_bfe_u32 v0, v54, 16, 1
	v_add3_u32 v0, v54, v0, s40
	v_bfe_u32 v52, v55, 16, 1
	v_lshrrev_b32_e32 v0, 16, v0
	v_add3_u32 v52, v55, v52, s40
	v_and_or_b32 v52, v52, s41, v0
	v_bfe_u32 v0, v56, 16, 1
	v_add3_u32 v0, v56, v0, s40
	v_bfe_u32 v53, v57, 16, 1
	v_lshrrev_b32_e32 v0, 16, v0
	v_add3_u32 v53, v57, v53, s40
	v_and_or_b32 v53, v53, s41, v0
	v_bfe_u32 v0, v58, 16, 1
	s_nop 0
	v_permlane32_swap_b32_e32 v50, v52
	v_permlane32_swap_b32_e32 v51, v53
	global_store_dwordx4 v[74:75], v[50:53], off offset:0
	s_nop 1
	v_add3_u32 v0, v58, v0, s40
	v_bfe_u32 v50, v59, 16, 1
	v_lshrrev_b32_e32 v0, 16, v0
	v_add3_u32 v50, v59, v50, s40
	v_and_or_b32 v50, v50, s41, v0
	v_bfe_u32 v0, v60, 16, 1
	v_add3_u32 v0, v60, v0, s40
	v_bfe_u32 v51, v61, 16, 1
	v_lshrrev_b32_e32 v0, 16, v0
	v_add3_u32 v51, v61, v51, s40
	v_and_or_b32 v51, v51, s41, v0
	v_bfe_u32 v0, v62, 16, 1
	v_add3_u32 v0, v62, v0, s40
	v_bfe_u32 v52, v63, 16, 1
	v_lshrrev_b32_e32 v0, 16, v0
	v_add3_u32 v52, v63, v52, s40
	v_and_or_b32 v52, v52, s41, v0
	v_bfe_u32 v0, v64, 16, 1
	v_add3_u32 v0, v64, v0, s40
	v_bfe_u32 v53, v65, 16, 1
	v_lshrrev_b32_e32 v0, 16, v0
	v_add3_u32 v53, v65, v53, s40
	v_and_or_b32 v53, v53, s41, v0
	v_bfe_u32 v0, v34, 16, 1
	v_add3_u32 v0, v34, v0, s40
	v_bfe_u32 v34, v35, 16, 1
	v_lshrrev_b32_e32 v0, 16, v0
	v_add3_u32 v34, v35, v34, s40
	v_and_or_b32 v34, v34, s41, v0
	v_bfe_u32 v0, v36, 16, 1
	v_add3_u32 v0, v36, v0, s40
	v_bfe_u32 v35, v37, 16, 1
	v_lshrrev_b32_e32 v0, 16, v0
	v_add3_u32 v35, v37, v35, s40
	v_and_or_b32 v35, v35, s41, v0
	v_bfe_u32 v0, v38, 16, 1
	v_add3_u32 v0, v38, v0, s40
	v_bfe_u32 v36, v39, 16, 1
	v_lshrrev_b32_e32 v0, 16, v0
	v_add3_u32 v36, v39, v36, s40
	v_and_or_b32 v36, v36, s41, v0
	v_bfe_u32 v0, v40, 16, 1
	v_add3_u32 v0, v40, v0, s40
	v_bfe_u32 v37, v41, 16, 1
	v_lshrrev_b32_e32 v0, 16, v0
	v_add3_u32 v37, v41, v37, s40
	v_and_or_b32 v37, v37, s41, v0
	v_bfe_u32 v0, v42, 16, 1
	s_nop 0
	v_permlane32_swap_b32_e32 v34, v36
	v_permlane32_swap_b32_e32 v35, v37
	global_store_dwordx4 v[74:75], v[34:37], off offset:64
	s_nop 1
	v_add3_u32 v0, v42, v0, s40
	v_bfe_u32 v34, v43, 16, 1
	v_lshrrev_b32_e32 v0, 16, v0
	v_add3_u32 v34, v43, v34, s40
; __device__ __forceinline__ unsigned pk2(float lo, float hi) { return f2bf(lo) | (f2bf(hi) << 16); }
; #define INP(k) ldptr(PTAB, (k))
; __device__ __forceinline__ void gla_g1(LAS unsigned char* lds, const bf16* Z, bf16* ST, float* DEC, const GlaPre pre, const float (&wa)[16], const float ba, int item, int tid) {
;     ...
;     bf16* stp = ST + ((size_t)item * 256 + 32 * wid + r32) * 128 + 4 * hf;
; #pragma unroll
;     for (int kt = 0; kt < 4; ++kt)
; #pragma unroll
;         for (int g = 0; g < 4; ++g) { v2u w; w.x = pk2(acc[kt][4 * g], acc[kt][4 * g + 1]); w.y = pk2(acc[kt][4 * g + 2], acc[kt][4 * g + 3]); *(v2u*)(stp + 32 * kt + 8 * g) = w; }
;     __syncthreads();
; __global__ void __launch_bounds__(NWAVES * 64, 2) fwd_kernel(Args args) {
;     ...
;               for (int it = vcu; it < 1024; it += G) { float wa[16], ba; gla_alpha_load(wa, ba, INP(6) + (size_t)l * 16 * 512, INP(7) + l * 512, (it >> 6) & 3, tid);
;                   const GlaPre cur = gla_blr_load(WSP(WS_ZABC), (size_t)(it >> 8) * SEQ + 64 * (it & 63), tid);
;                   gla_g1(ring, WSP(WS_ZABC), ((bf16*)xo), (float*)(ws + WS_GLADEC), cur, wa, ba, it, tid); } }
	v_and_or_b32 v34, v34, s41, v0
	v_bfe_u32 v0, v44, 16, 1
	v_add3_u32 v0, v44, v0, s40
	v_bfe_u32 v35, v45, 16, 1
	v_lshrrev_b32_e32 v0, 16, v0
	v_add3_u32 v35, v45, v35, s40
	v_and_or_b32 v35, v35, s41, v0
	v_bfe_u32 v0, v46, 16, 1
	v_add3_u32 v0, v46, v0, s40
	v_bfe_u32 v36, v47, 16, 1
	v_lshrrev_b32_e32 v0, 16, v0
	v_add3_u32 v36, v47, v36, s40
	v_and_or_b32 v36, v36, s41, v0
	v_bfe_u32 v0, v48, 16, 1
	v_add3_u32 v0, v48, v0, s40
	v_bfe_u32 v37, v49, 16, 1
	v_lshrrev_b32_e32 v0, 16, v0
	v_add3_u32 v37, v49, v37, s40
	v_and_or_b32 v37, v37, s41, v0
	v_bfe_u32 v0, v18, 16, 1
	v_add3_u32 v0, v18, v0, s40
	v_bfe_u32 v18, v19, 16, 1
	v_lshrrev_b32_e32 v0, 16, v0
	v_add3_u32 v18, v19, v18, s40
	v_and_or_b32 v18, v18, s41, v0
	v_bfe_u32 v0, v20, 16, 1
	v_add3_u32 v0, v20, v0, s40
	v_bfe_u32 v19, v21, 16, 1
	v_lshrrev_b32_e32 v0, 16, v0
	v_add3_u32 v19, v21, v19, s40
	v_and_or_b32 v19, v19, s41, v0
	v_bfe_u32 v0, v22, 16, 1
	v_add3_u32 v0, v22, v0, s40
	v_bfe_u32 v20, v23, 16, 1
	v_lshrrev_b32_e32 v0, 16, v0
	v_add3_u32 v20, v23, v20, s40
	v_and_or_b32 v20, v20, s41, v0
	v_bfe_u32 v0, v24, 16, 1
	v_add3_u32 v0, v24, v0, s40
	v_bfe_u32 v21, v25, 16, 1
	v_lshrrev_b32_e32 v0, 16, v0
	v_add3_u32 v21, v25, v21, s40
	v_and_or_b32 v21, v21, s41, v0
	v_bfe_u32 v0, v26, 16, 1
	s_nop 0
	v_permlane32_swap_b32_e32 v18, v20
	v_permlane32_swap_b32_e32 v19, v21
	global_store_dwordx4 v[74:75], v[18:21], off offset:128
	s_nop 1
	v_add3_u32 v0, v26, v0, s40
	v_bfe_u32 v18, v27, 16, 1
	v_lshrrev_b32_e32 v0, 16, v0
	v_add3_u32 v18, v27, v18, s40
	v_and_or_b32 v18, v18, s41, v0
	v_bfe_u32 v0, v28, 16, 1
	v_add3_u32 v0, v28, v0, s40
	v_bfe_u32 v19, v29, 16, 1
	v_lshrrev_b32_e32 v0, 16, v0
	v_add3_u32 v19, v29, v19, s40
	v_and_or_b32 v19, v19, s41, v0
	v_bfe_u32 v0, v30, 16, 1
	v_add3_u32 v0, v30, v0, s40
	v_bfe_u32 v20, v31, 16, 1
	v_lshrrev_b32_e32 v0, 16, v0
	v_add3_u32 v20, v31, v20, s40
	v_and_or_b32 v20, v20, s41, v0
	v_bfe_u32 v0, v32, 16, 1
	v_add3_u32 v0, v32, v0, s40
	v_bfe_u32 v21, v33, 16, 1
	v_lshrrev_b32_e32 v0, 16, v0
	v_add3_u32 v21, v33, v21, s40
	v_and_or_b32 v21, v21, s41, v0
	v_bfe_u32 v0, v2, 16, 1
	v_add3_u32 v0, v2, v0, s40
	v_bfe_u32 v2, v3, 16, 1
	v_lshrrev_b32_e32 v0, 16, v0
	v_add3_u32 v2, v3, v2, s40
	v_and_or_b32 v2, v2, s41, v0
	v_bfe_u32 v0, v4, 16, 1
	v_add3_u32 v0, v4, v0, s40
	v_bfe_u32 v3, v5, 16, 1
	v_lshrrev_b32_e32 v0, 16, v0
	v_add3_u32 v3, v5, v3, s40
	v_and_or_b32 v3, v3, s41, v0
	v_bfe_u32 v0, v6, 16, 1
	v_add3_u32 v0, v6, v0, s40
	v_bfe_u32 v4, v7, 16, 1
	v_lshrrev_b32_e32 v0, 16, v0
	v_add3_u32 v4, v7, v4, s40
	v_and_or_b32 v4, v4, s41, v0
	v_bfe_u32 v0, v8, 16, 1
	v_add3_u32 v0, v8, v0, s40
	v_bfe_u32 v5, v9, 16, 1
	v_lshrrev_b32_e32 v0, 16, v0
	v_add3_u32 v5, v9, v5, s40
	v_and_or_b32 v5, v5, s41, v0
	v_bfe_u32 v0, v10, 16, 1
	s_nop 0
	v_permlane32_swap_b32_e32 v2, v4
	v_permlane32_swap_b32_e32 v3, v5
	global_store_dwordx4 v[74:75], v[2:5], off offset:192
	s_nop 1
	v_add3_u32 v0, v10, v0, s40
	v_bfe_u32 v2, v11, 16, 1
	v_lshrrev_b32_e32 v0, 16, v0
	v_add3_u32 v2, v11, v2, s40
	v_and_or_b32 v2, v2, s41, v0
	v_bfe_u32 v0, v12, 16, 1
	v_add3_u32 v0, v12, v0, s40
	v_bfe_u32 v3, v13, 16, 1
	v_lshrrev_b32_e32 v0, 16, v0
	v_add3_u32 v3, v13, v3, s40
	v_and_or_b32 v3, v3, s41, v0
	v_bfe_u32 v0, v14, 16, 1
	v_readlane_b32 s14, v253, 59
	v_add3_u32 v0, v14, v0, s40
	v_bfe_u32 v4, v15, 16, 1
	s_add_i32 s0, s0, s14
	v_readlane_b32 s14, v254, 10
	v_lshrrev_b32_e32 v0, 16, v0
	v_add3_u32 v4, v15, v4, s40
	v_readlane_b32 s15, v254, 11
	s_add_u32 s12, s12, s14
	v_and_or_b32 v4, v4, s41, v0
	v_bfe_u32 v0, v16, 16, 1
	s_addc_u32 s13, s13, s15
	v_readlane_b32 s14, v255, 17
	v_add3_u32 v0, v16, v0, s40
	v_bfe_u32 v5, v17, 16, 1
	v_readlane_b32 s15, v255, 18
	s_add_u32 s10, s10, s14
	v_lshrrev_b32_e32 v0, 16, v0
	v_add3_u32 v5, v17, v5, s40
	s_addc_u32 s11, s11, s15
	v_and_or_b32 v5, v5, s41, v0
	s_cmpk_gt_i32 s1, 0x3ff
	s_nop 1
	v_permlane32_swap_b32_e32 v50, v52
	v_permlane32_swap_b32_e32 v51, v53
	global_store_dwordx4 v[74:75], v[50:53], off offset:32
	v_permlane32_swap_b32_e32 v34, v36
	v_permlane32_swap_b32_e32 v35, v37
	global_store_dwordx4 v[74:75], v[34:37], off offset:96
	v_permlane32_swap_b32_e32 v18, v20
	v_permlane32_swap_b32_e32 v19, v21
	global_store_dwordx4 v[74:75], v[18:21], off offset:160
	v_permlane32_swap_b32_e32 v2, v4
	v_permlane32_swap_b32_e32 v3, v5
	global_store_dwordx4 v[74:75], v[2:5], off offset:224
	s_barrier
	s_cbranch_scc1 .LBB0_924

; #define LAS __attribute__((address_space(3)))
; __device__ __forceinline__ unsigned pk2(float lo, float hi) { return f2bf(lo) | (f2bf(hi) << 16); }
; __device__ __forceinline__ float bflo(unsigned w) { return __uint_as_float(w << 16); }
; __device__ __forceinline__ float bfhi(unsigned w) { return __uint_as_float(w & 0xffff0000u); }
; __device__ __forceinline__ void gla_cum(LAS unsigned char* lds, const GlaPre pre, const float (&wa)[16], const float ba, int tid) {
;     ...
;     tot[q * 128 + k] = run;
;     __syncthreads();
;     float off = 0.f;
; #pragma unroll
;     for (int qq = 0; qq < 3; ++qq) off += (qq < q) ? tot[qq * 128 + k] : 0.f;
; #pragma unroll
;     for (int i = 0; i < 16; ++i) cum[(16 * q + i) * 128 + k] = c[i] + off;
;     __syncthreads();
; __device__ __forceinline__ void gla_g3(LAS unsigned char* lds, const bf16* Z, const bf16* ST, bf16* Oabc, const GlaPre pre, const float (&wa)[16], const float ba, const float* gla_norm, int item, int tid) {
;     ...
;     for (int i = 0; i < 2; ++i) { const int t = (tid >> 4) + 32 * i, kc = (tid & 15) * 8;
;         const v4u qw = qraw[i], kw = kraw[i];
;         const f32x4 c0 = *(const LAS f32x4*)(cum + t * 128 + kc), c1 = *(const LAS f32x4*)(cum + t * 128 + kc + 4);
;         const float e[8] = {__expf(c0.x), __expf(c0.y), __expf(c0.z), __expf(c0.w), __expf(c1.x), __expf(c1.y), __expf(c1.z), __expf(c1.w)};
;         const float ei[8] = {__expf(-c0.x), __expf(-c0.y), __expf(-c0.z), __expf(-c0.w), __expf(-c1.x), __expf(-c1.y), __expf(-c1.z), __expf(-c1.w)};
;         v4u qo, ko;
;         qo.x = pk2(bflo(qw.x) * qscale * e[0], bfhi(qw.x) * qscale * e[1]); qo.y = pk2(bflo(qw.y) * qscale * e[2], bfhi(qw.y) * qscale * e[3]);
;         qo.z = pk2(bflo(qw.z) * qscale * e[4], bfhi(qw.z) * qscale * e[5]); qo.w = pk2(bflo(qw.w) * qscale * e[6], bfhi(qw.w) * qscale * e[7]);
;         ko.x = pk2(bflo(kw.x) * ei[0], bfhi(kw.x) * ei[1]); ko.y = pk2(bflo(kw.y) * ei[2], bfhi(kw.y) * ei[3]);
;         ko.z = pk2(bflo(kw.z) * ei[4], bfhi(kw.z) * ei[5]); ko.w = pk2(bflo(kw.w) * ei[6], bfhi(kw.w) * ei[7]);
;         *(LAS v4u*)(lds + GL_QD + KSWZ256(t, kc * 2)) = qo; *(LAS v4u*)(lds + GL_KI + KSWZ256(t, kc * 2)) = ko; }
.LBB0_1110:
	s_or_b64 exec, exec, s[38:39]
	v_readlane_b32 s8, v252, 6
	v_readlane_b32 s4, v252, 4
	v_readlane_b32 s14, v252, 12
	v_readlane_b32 s15, v252, 13
	v_readlane_b32 s0, v252, 32
	v_readlane_b32 s5, v252, 5
	s_mov_b64 s[6:7], s[14:15]
	v_readlane_b32 s1, v252, 33
	s_waitcnt lgkmcnt(0)
	s_barrier
	v_mbcnt_lo_u32_b32 v0, -1, 0
	v_mbcnt_hi_u32_b32 v0, -1, v0
	s_and_b64 vcc, exec, s[0:1]
	v_readlane_b32 s9, v252, 7
	v_readlane_b32 s10, v252, 8
	v_readlane_b32 s11, v252, 9
	v_readlane_b32 s12, v252, 10
	v_readlane_b32 s13, v252, 11
	v_mbcnt_lo_u32_b32 v0, -1, 0
	v_mbcnt_hi_u32_b32 v0, -1, v0
	s_cbranch_vccz .LBB0_1119
	v_readlane_b32 s0, v255, 23
	s_lshl_b32 s94, s0, 10
	s_add_u32 s8, s4, 0x15600000
	v_readlane_b32 s0, v252, 37
	s_addc_u32 s9, s5, 0
	v_readlane_b32 s1, v255, 24
	v_add_u32_e32 v136, s0, v0
	s_add_u32 s0, s4, 0x29e00000
	v_ashrrev_i32_e32 v130, 4, v136
	v_and_b32_e32 v0, 15, v0
	s_addc_u32 s1, s5, 0
	v_readlane_b32 s12, v254, 8
	v_readlane_b32 s4, v254, 12
	v_and_b32_e32 v137, 0x7f, v136
	v_ashrrev_i32_e32 v131, 31, v130
	v_lshlrev_b32_e32 v132, 1, v0
	s_lshl_b64 s[10:11], s[94:95], 2
	v_readlane_b32 s13, v254, 9
	v_readlane_b32 s16, v253, 58
	s_mov_b32 s17, s4
	v_readlane_b32 s5, v254, 13
	v_readlane_b32 s98, v252, 37
	s_nop 3
	s_cmpk_lt_u32 s98, 0x100
	s_cbranch_scc1 .Lprio_g3_done
	s_setprio 1
.Lprio_g3_done:
	s_branch .LBB0_1113
.LBB0_1112:
	s_or_b64 exec, exec, s[14:15]
	s_waitcnt lgkmcnt(0)
	v_add_f32_e32 v36, v36, v76
	v_add_f32_e32 v36, v36, v38
	v_lshlrev_b32_e32 v37, 13, v55
	v_lshlrev_b32_e32 v35, 2, v35
	v_add3_u32 v35, 0, v37, v35
	v_add_f32_e32 v37, v77, v36
	v_add_f32_e32 v38, v78, v36
	ds_write2st64_b32 v35, v37, v38 offset1:2
	v_add_f32_e32 v37, v79, v36
	v_add_f32_e32 v38, v80, v36
	ds_write2st64_b32 v35, v37, v38 offset0:4 offset1:6
	v_add_f32_e32 v37, v82, v36
	v_add_f32_e32 v38, v83, v36
	ds_write2st64_b32 v35, v37, v38 offset0:8 offset1:10
	v_add_f32_e32 v37, v84, v36
	v_add_f32_e32 v38, v85, v36
	ds_write2st64_b32 v35, v37, v38 offset0:12 offset1:14
	v_add_f32_e32 v37, v86, v36
	v_add_f32_e32 v38, v87, v36
	ds_write2st64_b32 v35, v37, v38 offset0:16 offset1:18
	v_add_f32_e32 v37, v88, v36
	v_add_f32_e32 v38, v42, v36
	ds_write2st64_b32 v35, v37, v38 offset0:20 offset1:22
	v_add_f32_e32 v37, v43, v36
	v_add_f32_e32 v38, v44, v36
	v_lshl_add_u32 v55, v58, 2, 0
	ds_write2st64_b32 v35, v37, v38 offset0:24 offset1:26
	v_add_f32_e32 v37, v45, v36
	v_add_f32_e32 v34, v34, v36
	v_lshl_add_u32 v38, v56, 9, v55
	ds_write2st64_b32 v35, v37, v34 offset0:28 offset1:30
	s_waitcnt lgkmcnt(0)
	s_barrier
	ds_read_b128 v[34:37], v38
	ds_read_b128 v[38:41], v38 offset:16
	s_add_u32 s14, s20, s10
	s_mov_b32 s20, 0x3db504f3
	v_and_b32_e32 v57, 0x70, v133
	s_waitcnt lgkmcnt(1)
	v_mul_f32_e32 v43, 0x3fb8aa3b, v35
	s_waitcnt lgkmcnt(0)
	v_mul_f32_e32 v59, 0x3fb8aa3b, v38
	v_mul_f32_e32 v42, 0x3fb8aa3b, v34
	v_exp_f32_e32 v44, v43
	v_mul_f32_e32 v43, 0x3fb8aa3b, v36
	v_exp_f32_e32 v60, v59
	v_mul_f32_e32 v59, 0x3fb8aa3b, v39
	v_exp_f32_e32 v42, v42
	v_exp_f32_e32 v43, v43
	v_exp_f32_e32 v62, v59
	v_mul_f32_e32 v59, 0x3fb8aa3b, v40
	v_mul_f32_e32 v35, 0xbfb8aa3b, v35
	v_mul_f32_e32 v45, 0x3fb8aa3b, v37
	v_exp_f32_e32 v61, v59
	v_mul_f32_e32 v59, 0x3fb8aa3b, v41
	v_exp_f32_e32 v64, v35
	v_mul_f32_e32 v35, 0xbfb8aa3b, v36
	v_mul_f32_e32 v36, 0xbfb8aa3b, v37
	v_mul_f32_e32 v37, 0xbfb8aa3b, v39
	v_exp_f32_e32 v63, v59
	v_exp_f32_e32 v65, v36
	v_mul_f32_e32 v36, 0xbfb8aa3b, v38
	v_exp_f32_e32 v38, v37
	v_mul_f32_e32 v37, 0xbfb8aa3b, v40
	v_mul_f32_e32 v39, 0xbfb8aa3b, v41
	s_waitcnt vmcnt(7)
	v_lshlrev_b32_e32 v41, 16, v31
	v_lshlrev_b32_e32 v40, 16, v30
	v_exp_f32_e32 v45, v45
	v_pk_mul_f32 v[40:41], v[40:41], s[20:21] op_sel_hi:[1,0]
	v_and_b32_e32 v31, 0xffff0000, v31
	v_pk_mul_f32 v[40:41], v[40:41], v[42:43]
	v_lshlrev_b32_e32 v43, 16, v33
	v_lshlrev_b32_e32 v42, 16, v32
	v_and_b32_e32 v33, 0xffff0000, v33
	v_and_b32_e32 v32, 0xffff0000, v32
	v_and_b32_e32 v30, 0xffff0000, v30
	v_pk_mul_f32 v[32:33], v[32:33], s[20:21] op_sel_hi:[1,0]
	v_pk_mul_f32 v[30:31], v[30:31], s[20:21] op_sel_hi:[1,0]
	v_pk_mul_f32 v[32:33], v[32:33], v[62:63]
	v_mul_f32_e32 v34, 0xbfb8aa3b, v34
	v_pk_mul_f32 v[30:31], v[30:31], v[44:45]
	v_bfe_u32 v44, v33, 16, 1
	v_bfe_u32 v45, v32, 16, 1
	v_exp_f32_e32 v34, v34
	v_exp_f32_e32 v35, v35
	v_pk_mul_f32 v[42:43], v[42:43], s[20:21] op_sel_hi:[1,0]
	v_add3_u32 v32, v32, v45, s40
	v_add3_u32 v33, v33, v44, s40
	v_bfe_u32 v44, v40, 16, 1
	v_bfe_u32 v45, v41, 16, 1
	v_exp_f32_e32 v39, v39
	v_pk_mul_f32 v[42:43], v[42:43], v[60:61]
	v_bfe_u32 v59, v31, 16, 1
	v_bfe_u32 v60, v30, 16, 1
	v_add3_u32 v41, v41, v45, s40
	v_add3_u32 v40, v40, v44, s40
	v_add3_u32 v30, v30, v60, s40
	v_add3_u32 v31, v31, v59, s40
	v_lshrrev_b32_e32 v40, 16, v40
	v_lshrrev_b32_e32 v41, 16, v41
	v_and_or_b32 v31, v31, s41, v41
	v_and_or_b32 v30, v30, s41, v40
	s_waitcnt vmcnt(6)
; #define LAS __attribute__((address_space(3)))
; __device__ __forceinline__ unsigned pk2(float lo, float hi) { return f2bf(lo) | (f2bf(hi) << 16); }
; __device__ __forceinline__ float bflo(unsigned w) { return __uint_as_float(w << 16); }
; __device__ __forceinline__ float bfhi(unsigned w) { return __uint_as_float(w & 0xffff0000u); }
; __device__ __forceinline__ int v_st(int k, int c) { const int kk = (k & ~0xC) | ((k & 4) << 1) | ((k & 8) >> 1); return ((kk >> 3) * 4 + (c >> 5)) * 512 + ((kk & 7) * 32 + (c & 31)) * 2; }
; __device__ __forceinline__ void gla_write_v(LAS unsigned char* lds, const GlaV& v, int tid) {
; #pragma unroll
;     for (int i = 0; i < 4; ++i) { const int piece = tid + 512 * i, t = piece >> 5, cc = (piece & 31) * 8; *(LAS v4u*)(lds + GL_V + (cc >> 7) * 16384 + fa::v_st(t, cc & 127)) = v.w[i]; }
; }
; __device__ __forceinline__ void gla_g3(LAS unsigned char* lds, const bf16* Z, const bf16* ST, bf16* Oabc, const GlaPre pre, const float (&wa)[16], const float ba, const float* gla_norm, int item, int tid) {
;     ...
;     for (int i = 0; i < 2; ++i) { const int t = (tid >> 4) + 32 * i, kc = (tid & 15) * 8;
;         const v4u qw = qraw[i], kw = kraw[i];
;         const f32x4 c0 = *(const LAS f32x4*)(cum + t * 128 + kc), c1 = *(const LAS f32x4*)(cum + t * 128 + kc + 4);
;         const float e[8] = {__expf(c0.x), __expf(c0.y), __expf(c0.z), __expf(c0.w), __expf(c1.x), __expf(c1.y), __expf(c1.z), __expf(c1.w)};
;         const float ei[8] = {__expf(-c0.x), __expf(-c0.y), __expf(-c0.z), __expf(-c0.w), __expf(-c1.x), __expf(-c1.y), __expf(-c1.z), __expf(-c1.w)};
;         v4u qo, ko;
;         qo.x = pk2(bflo(qw.x) * qscale * e[0], bfhi(qw.x) * qscale * e[1]); qo.y = pk2(bflo(qw.y) * qscale * e[2], bfhi(qw.y) * qscale * e[3]);
;         qo.z = pk2(bflo(qw.z) * qscale * e[4], bfhi(qw.z) * qscale * e[5]); qo.w = pk2(bflo(qw.w) * qscale * e[6], bfhi(qw.w) * qscale * e[7]);
;         ko.x = pk2(bflo(kw.x) * ei[0], bfhi(kw.x) * ei[1]); ko.y = pk2(bflo(kw.y) * ei[2], bfhi(kw.y) * ei[3]);
;         ko.z = pk2(bflo(kw.z) * ei[4], bfhi(kw.z) * ei[5]); ko.w = pk2(bflo(kw.w) * ei[6], bfhi(kw.w) * ei[7]);
;         *(LAS v4u*)(lds + GL_QD + KSWZ256(t, kc * 2)) = qo; *(LAS v4u*)(lds + GL_KI + KSWZ256(t, kc * 2)) = ko; }
	v_lshlrev_b32_e32 v41, 16, v27
	v_lshlrev_b32_e32 v40, 16, v26
	v_exp_f32_e32 v36, v36
	v_exp_f32_e32 v37, v37
	v_pk_mul_f32 v[34:35], v[34:35], v[40:41]
	v_lshlrev_b32_e32 v41, 16, v29
	v_lshlrev_b32_e32 v40, 16, v28
	v_and_b32_e32 v29, 0xffff0000, v29
	v_and_b32_e32 v28, 0xffff0000, v28
	v_pk_mul_f32 v[28:29], v[38:39], v[28:29]
	v_and_b32_e32 v27, 0xffff0000, v27
	v_and_b32_e32 v26, 0xffff0000, v26
	v_bfe_u32 v38, v29, 16, 1
	v_pk_mul_f32 v[26:27], v[64:65], v[26:27]
	v_add3_u32 v29, v29, v38, s40
	v_bfe_u32 v38, v34, 16, 1
	v_pk_mul_f32 v[36:37], v[36:37], v[40:41]
	v_bfe_u32 v41, v26, 16, 1
	v_add3_u32 v34, v34, v38, s40
	v_bfe_u32 v59, v42, 16, 1
	v_bfe_u32 v60, v43, 16, 1
	v_bfe_u32 v39, v28, 16, 1
	v_bfe_u32 v40, v27, 16, 1
	v_add3_u32 v26, v26, v41, s40
	v_lshrrev_b32_e32 v34, 16, v34
	v_add3_u32 v43, v43, v60, s40
	v_add3_u32 v42, v42, v59, s40
	v_add3_u32 v27, v27, v40, s40
	v_add3_u32 v28, v28, v39, s40
	v_bfe_u32 v39, v35, 16, 1
	v_bfe_u32 v40, v36, 16, 1
	v_bfe_u32 v41, v37, 16, 1
	v_and_or_b32 v26, v26, s41, v34
	v_lshlrev_b32_e32 v34, 8, v56
	v_lshrrev_b32_e32 v42, 16, v42
	v_lshrrev_b32_e32 v43, 16, v43
	v_add3_u32 v37, v37, v41, s40
	v_add3_u32 v36, v36, v40, s40
	v_add3_u32 v35, v35, v39, s40
	v_bitop3_b32 v34, v0, v34, v57 bitop3:0xde
	v_and_or_b32 v33, v33, s41, v43
	v_and_or_b32 v32, v32, s41, v42
	v_lshrrev_b32_e32 v35, 16, v35
	v_lshrrev_b32_e32 v36, 16, v36
	v_lshrrev_b32_e32 v37, 16, v37
	v_add_u32_e32 v34, 0, v34
	v_and_or_b32 v29, v29, s41, v37
	v_and_or_b32 v28, v28, s41, v36
	v_and_or_b32 v27, v27, s41, v35
	ds_write_b128 v34, v[30:33] offset:32768
	ds_write_b128 v34, v[26:29] offset:49152
	v_lshl_add_u32 v30, v48, 9, v55
	ds_read_b128 v[26:29], v30
	ds_read_b128 v[30:33], v30 offset:16
	s_addc_u32 s15, s19, s11
	s_ashr_i32 s21, s18, 6
	s_add_i32 s19, 0, 0x10000
	s_waitcnt lgkmcnt(1)
	v_mul_f32_e32 v35, 0x3fb8aa3b, v27
	v_mul_f32_e32 v34, 0x3fb8aa3b, v26
	v_exp_f32_e32 v36, v35
	v_mul_f32_e32 v35, 0x3fb8aa3b, v28
	v_exp_f32_e32 v34, v34
	v_exp_f32_e32 v35, v35
	v_mul_f32_e32 v27, 0xbfb8aa3b, v27
	v_mul_f32_e32 v37, 0x3fb8aa3b, v29
	s_waitcnt lgkmcnt(0)
	v_mul_f32_e32 v39, 0x3fb8aa3b, v31
	v_mul_f32_e32 v41, 0x3fb8aa3b, v33
	v_exp_f32_e32 v42, v27
	v_mul_f32_e32 v27, 0xbfb8aa3b, v28
	v_mul_f32_e32 v28, 0xbfb8aa3b, v29
	v_mul_f32_e32 v29, 0xbfb8aa3b, v31
	v_mul_f32_e32 v38, 0x3fb8aa3b, v30
	v_exp_f32_e32 v40, v39
	v_mul_f32_e32 v39, 0x3fb8aa3b, v32
	v_exp_f32_e32 v41, v41
	v_exp_f32_e32 v43, v28
	v_mul_f32_e32 v28, 0xbfb8aa3b, v30
	v_exp_f32_e32 v30, v29
	v_mul_f32_e32 v29, 0xbfb8aa3b, v32
	v_mul_f32_e32 v31, 0xbfb8aa3b, v33
	s_waitcnt vmcnt(5)
	v_lshlrev_b32_e32 v33, 16, v23
	v_lshlrev_b32_e32 v32, 16, v22
	v_exp_f32_e32 v37, v37
	v_pk_mul_f32 v[32:33], v[32:33], s[20:21] op_sel_hi:[1,0]
	v_exp_f32_e32 v38, v38
	v_pk_mul_f32 v[32:33], v[32:33], v[34:35]
	v_lshlrev_b32_e32 v35, 16, v25
	v_lshlrev_b32_e32 v34, 16, v24
	v_and_b32_e32 v25, 0xffff0000, v25
	v_and_b32_e32 v24, 0xffff0000, v24
	v_exp_f32_e32 v39, v39
	v_and_b32_e32 v23, 0xffff0000, v23
	v_and_b32_e32 v22, 0xffff0000, v22
	v_pk_mul_f32 v[24:25], v[24:25], s[20:21] op_sel_hi:[1,0]
	v_pk_mul_f32 v[22:23], v[22:23], s[20:21] op_sel_hi:[1,0]
	v_pk_mul_f32 v[24:25], v[24:25], v[40:41]
	v_mul_f32_e32 v26, 0xbfb8aa3b, v26
	v_pk_mul_f32 v[22:23], v[22:23], v[36:37]
	v_bfe_u32 v36, v25, 16, 1
	v_bfe_u32 v37, v24, 16, 1
	v_exp_f32_e32 v26, v26
	v_exp_f32_e32 v27, v27
	v_pk_mul_f32 v[34:35], v[34:35], s[20:21] op_sel_hi:[1,0]
	v_add3_u32 v24, v24, v37, s40
	v_add3_u32 v25, v25, v36, s40
	v_bfe_u32 v36, v32, 16, 1
	v_bfe_u32 v37, v33, 16, 1
	v_exp_f32_e32 v31, v31
	v_pk_mul_f32 v[34:35], v[34:35], v[38:39]
	v_bfe_u32 v38, v23, 16, 1
	v_bfe_u32 v39, v22, 16, 1
	v_add3_u32 v33, v33, v37, s40
	v_add3_u32 v32, v32, v36, s40
	v_add3_u32 v22, v22, v39, s40
	v_add3_u32 v23, v23, v38, s40
	v_lshrrev_b32_e32 v32, 16, v32
	v_lshrrev_b32_e32 v33, 16, v33
	v_and_or_b32 v23, v23, s41, v33
	v_and_or_b32 v22, v22, s41, v32
	s_waitcnt vmcnt(4)
	v_lshlrev_b32_e32 v33, 16, v19
	v_lshlrev_b32_e32 v32, 16, v18
	v_exp_f32_e32 v28, v28
	v_exp_f32_e32 v29, v29
	v_pk_mul_f32 v[26:27], v[26:27], v[32:33]
	v_lshlrev_b32_e32 v33, 16, v21
	v_lshlrev_b32_e32 v32, 16, v20
	v_and_b32_e32 v21, 0xffff0000, v21
	v_and_b32_e32 v20, 0xffff0000, v20
	v_pk_mul_f32 v[20:21], v[30:31], v[20:21]
	v_and_b32_e32 v19, 0xffff0000, v19
	v_and_b32_e32 v18, 0xffff0000, v18
	v_bfe_u32 v30, v21, 16, 1
	v_pk_mul_f32 v[18:19], v[42:43], v[18:19]
	v_add3_u32 v21, v21, v30, s40
	v_bfe_u32 v30, v26, 16, 1
	v_pk_mul_f32 v[28:29], v[28:29], v[32:33]
	v_bfe_u32 v32, v19, 16, 1
	v_bfe_u32 v33, v18, 16, 1
	v_add3_u32 v26, v26, v30, s40
	v_bfe_u32 v38, v34, 16, 1
	v_bfe_u32 v39, v35, 16, 1
	v_bfe_u32 v31, v20, 16, 1
	v_add3_u32 v18, v18, v33, s40
	v_add3_u32 v19, v19, v32, s40
	v_bfe_u32 v32, v28, 16, 1
	v_bfe_u32 v33, v29, 16, 1
	v_lshrrev_b32_e32 v26, 16, v26
	v_add3_u32 v35, v35, v39, s40
	v_add3_u32 v34, v34, v38, s40
	v_add3_u32 v20, v20, v31, s40
	v_bfe_u32 v31, v27, 16, 1
	v_add3_u32 v29, v29, v33, s40
	v_add3_u32 v28, v28, v32, s40
	v_and_or_b32 v18, v18, s41, v26
	v_lshlrev_b32_e32 v26, 8, v48
	v_lshrrev_b32_e32 v34, 16, v34
	v_lshrrev_b32_e32 v35, 16, v35
	v_add3_u32 v27, v27, v31, s40
	v_lshrrev_b32_e32 v28, 16, v28
	v_lshrrev_b32_e32 v29, 16, v29
	v_bitop3_b32 v26, v0, v26, v57 bitop3:0xde
	v_and_or_b32 v25, v25, s41, v35
	v_and_or_b32 v24, v24, s41, v34
	v_lshrrev_b32_e32 v27, 16, v27
	v_and_or_b32 v21, v21, s41, v29
	v_and_or_b32 v20, v20, s41, v28
	v_add_u32_e32 v26, 0, v26
	v_and_or_b32 v19, v19, s41, v27
	ds_write_b128 v26, v[22:25] offset:32768
	ds_write_b128 v26, v[18:21] offset:49152
	v_and_b32_e32 v20, 0xfffff0, v46
	v_lshlrev_b32_e32 v21, 1, v46
	v_lshlrev_b32_e32 v18, 10, v133
	v_and_or_b32 v20, v21, 8, v20
	v_and_b32_e32 v18, 0x4000, v18
	v_lshrrev_b32_e32 v19, 5, v58
	v_lshrrev_b32_e32 v21, 1, v46
	v_lshrrev_b32_e32 v20, 1, v20
	v_bfe_u32 v22, v133, 5, 2
	v_add_u32_e32 v18, s19, v18
	v_or_b32_e32 v20, v20, v19
	v_and_or_b32 v21, v21, 4, v22
	v_and_b32_e32 v0, 48, v0
	v_lshlrev_b32_e32 v21, 6, v21
	v_lshl_add_u32 v20, v20, 9, v18
	v_add3_u32 v20, v20, v21, v0
	s_waitcnt vmcnt(3)
; #define LAS __attribute__((address_space(3)))
; __device__ __forceinline__ void gla_g3(LAS unsigned char* lds, const bf16* Z, const bf16* ST, bf16* Oabc, const GlaPre pre, const float (&wa)[16], const float ba, const float* gla_norm, int item, int tid) {
;     ...
;     const int ri = wid & 1, cq = wid >> 1;
;     bf16x8 qf[8];
; #pragma unroll
;     for (int d0 = 0; d0 < 8; ++d0) qf[d0] = *(const LAS bf16x8*)(lds + GL_QD + KSWZ256(32 * ri + r32, (d0 * 16 + hf * 8) * 2));
;     bf16x8 sfr[2][8];
; #pragma unroll
;     for (int dd = 0; dd < 2; ++dd) { const bf16* sp = ST + ((size_t)item * 256 + 64 * cq + 32 * dd + r32) * 128 + hf * 8;
; #pragma unroll
;         for (int d0 = 0; d0 < 8; ++d0) sfr[dd][d0] = *(const bf16x8*)(sp + d0 * 16); }
;     f32x16 p0, p1;
; #pragma unroll
;     for (int r = 0; r < 16; ++r) { p0[r] = 0.f; p1[r] = 0.f; }
; #pragma unroll
;     for (int d0 = 0; d0 < 8; ++d0) {
;         const bf16x8 a0 = *(const LAS bf16x8*)(lds + GL_KI + KSWZ256(r32, (d0 * 16 + hf * 8) * 2)), a1 = *(const LAS bf16x8*)(lds + GL_KI + KSWZ256(32 + r32, (d0 * 16 + hf * 8) * 2));
;         p0 = __builtin_amdgcn_mfma_f32_32x32x16_bf16(a0, qf[d0], p0, 0, 0, 0);
;         p1 = __builtin_amdgcn_mfma_f32_32x32x16_bf16(a1, qf[d0], p1, 0, 0, 0); }
	ds_write_b128 v20, v[2:5]
	v_and_b32_e32 v2, 0xfffff0, v50
	v_lshlrev_b32_e32 v3, 1, v50
	v_and_or_b32 v2, v3, 8, v2
	v_lshrrev_b32_e32 v3, 1, v50
	v_lshrrev_b32_e32 v2, 1, v2
	v_bfe_u32 v4, v49, 5, 2
	v_or_b32_e32 v2, v2, v19
	v_and_or_b32 v3, v3, 4, v4
	v_lshlrev_b32_e32 v3, 6, v3
	v_lshl_add_u32 v2, v2, 9, v18
	v_add3_u32 v2, v2, v3, v0
	s_waitcnt vmcnt(2)
	ds_write_b128 v2, v[6:9]
	v_and_b32_e32 v2, 0xfffff0, v52
	v_lshlrev_b32_e32 v3, 1, v52
	v_and_or_b32 v2, v3, 8, v2
	v_lshrrev_b32_e32 v3, 1, v52
	v_lshrrev_b32_e32 v2, 1, v2
	v_bfe_u32 v4, v51, 5, 2
	v_or_b32_e32 v2, v2, v19
	v_and_or_b32 v3, v3, 4, v4
	v_lshlrev_b32_e32 v3, 6, v3
	v_lshl_add_u32 v2, v2, 9, v18
	v_add3_u32 v2, v2, v3, v0
	s_waitcnt vmcnt(1)
	ds_write_b128 v2, v[10:13]
	v_and_b32_e32 v2, 0xfffff0, v54
	v_lshlrev_b32_e32 v3, 1, v54
	v_and_or_b32 v2, v3, 8, v2
	v_lshrrev_b32_e32 v3, 1, v54
	v_lshrrev_b32_e32 v2, 1, v2
	v_bfe_u32 v4, v53, 5, 2
	v_or_b32_e32 v2, v2, v19
	v_and_or_b32 v3, v3, 4, v4
	v_lshlrev_b32_e32 v3, 6, v3
	v_lshl_add_u32 v2, v2, 9, v18
	v_bfe_u32 v142, v133, 5, 1
	v_and_b32_e32 v134, 31, v133
	v_add3_u32 v0, v2, v3, v0
	s_waitcnt vmcnt(0)
	ds_write_b128 v0, v[14:17]
	v_lshlrev_b32_e32 v6, 8, v134
	v_lshlrev_b32_e32 v0, 4, v142
	s_movk_i32 s23, 0x70
	v_bitop3_b32 v7, v0, v47, s23 bitop3:0x78
	v_add_u32_e32 v88, 0, v6
	s_and_b32 s22, s21, 1
	v_add_u32_e32 v8, v88, v7
	s_waitcnt lgkmcnt(0)
	s_barrier
	s_lshl_b32 s20, s22, 13
	ds_read_b128 v[2:5], v8 offset:49152
	s_add_i32 s20, s20, 0
	v_add_u32_e32 v67, s20, v6
	v_add_u32_e32 v6, v67, v7
	ds_read_b128 v[34:37], v6 offset:32768
	v_and_b32_e32 v66, 0x70, v47
	v_bitop3_b32 v42, v0, v66, 32 bitop3:0x36
	v_add_u32_e32 v6, v67, v42
	ds_read_b128 v[38:41], v6 offset:32768
	ds_read_b128 v[18:21], v8 offset:57344
	s_waitcnt lgkmcnt(2)
	v_mfma_f32_32x32x16_bf16 v[2:17], v[2:5], v[34:37], 0
	v_add_u32_e32 v46, v88, v42
	ds_read_b128 v[42:45], v46 offset:49152
	ds_read_b128 v[46:49], v46 offset:57344
	s_movk_i32 s20, 0x60
	v_bitop3_b32 v58, v0, v66, s20 bitop3:0x36
	s_movk_i32 s20, 0x80
	v_mov_b32_e32 v135, v1
	v_and_b32_e32 v150, 63, v133
	s_waitcnt lgkmcnt(2)
	v_mfma_f32_32x32x16_bf16 v[18:33], v[18:21], v[34:37], 0
	v_lshlrev_b32_e32 v162, 4, v150
	s_waitcnt lgkmcnt(1)
	v_mfma_f32_32x32x16_bf16 v[2:17], v[42:45], v[38:41], v[2:17]
	v_bitop3_b32 v42, v0, v66, 64 bitop3:0x36
	v_add_u32_e32 v54, v88, v42
	ds_read_b128 v[50:53], v54 offset:49152
	v_add_u32_e32 v42, v67, v42
	ds_read_b128 v[42:45], v42 offset:32768
	s_waitcnt lgkmcnt(2)
	v_mfma_f32_32x32x16_bf16 v[18:33], v[46:49], v[38:41], v[18:33]
	v_add_u32_e32 v46, v67, v58
	ds_read_b128 v[46:49], v46 offset:32768
	ds_read_b128 v[54:57], v54 offset:57344
	s_waitcnt lgkmcnt(2)
	v_mfma_f32_32x32x16_bf16 v[2:17], v[50:53], v[42:45], v[2:17]
	s_waitcnt lgkmcnt(0)
	v_mfma_f32_32x32x16_bf16 v[18:33], v[54:57], v[42:45], v[18:33]
	v_add_u32_e32 v54, v88, v58
	ds_read_b128 v[50:53], v54 offset:49152
	ds_read_b128 v[54:57], v54 offset:57344
	s_waitcnt lgkmcnt(1)
	v_mfma_f32_32x32x16_bf16 v[2:17], v[50:53], v[46:49], v[2:17]
	v_bitop3_b32 v50, v0, v66, s20 bitop3:0x36
	v_add_u32_e32 v62, v88, v50
	ds_read_b128 v[58:61], v62 offset:49152
	s_movk_i32 s20, 0xa0
	v_bitop3_b32 v68, v0, v66, s20 bitop3:0x36
	v_add_u32_e32 v50, v67, v50
	ds_read_b128 v[50:53], v50 offset:32768
	s_waitcnt lgkmcnt(2)
	v_mfma_f32_32x32x16_bf16 v[18:33], v[54:57], v[46:49], v[18:33]
	v_add_u32_e32 v54, v67, v68
	ds_read_b128 v[54:57], v54 offset:32768
	ds_read_b128 v[62:65], v62 offset:57344
	s_movk_i32 s20, 0xc0
	v_bitop3_b32 v70, v0, v66, s20 bitop3:0x36
	s_movk_i32 s20, 0xe0
	v_bitop3_b32 v89, v0, v66, s20 bitop3:0x36
	v_add_u32_e32 v71, v67, v89
	s_waitcnt lgkmcnt(0)
	v_mfma_f32_32x32x16_bf16 v[18:33], v[62:65], v[50:53], v[18:33]
	v_add_u32_e32 v62, v88, v68
	v_add_u32_e32 v63, v67, v70
	ds_read_b128 v[66:69], v62 offset:57344
	v_add_u32_e32 v74, v88, v70
	s_ashr_i32 s20, s18, 7
	s_lshl_b32 s23, s20, 6
	s_ashr_i32 s25, s23, 31
	v_mfma_f32_32x32x16_bf16 v[2:17], v[58:61], v[50:53], v[2:17]
	ds_read_b128 v[58:61], v62 offset:49152
	s_add_u32 s24, s12, s23
	s_addc_u32 s25, s13, s25
	s_lshl_b32 s22, s22, 5
	s_lshl_b32 s18, s18, 6
	s_and_b32 s18, s18, 0xffffc000
	s_add_i32 s18, s18, s19
	s_waitcnt lgkmcnt(0)
	v_mfma_f32_32x32x16_bf16 v[2:17], v[58:61], v[54:57], v[2:17]
	ds_read_b128 v[62:65], v63 offset:32768
	ds_read_b128 v[58:61], v71 offset:32768
	ds_read_b128 v[70:73], v74 offset:49152
	v_mfma_f32_32x32x16_bf16 v[18:33], v[66:69], v[54:57], v[18:33]
	v_lshl_add_u64 v[66:67], s[24:25], 0, v[134:135]
	v_lshl_add_u64 v[68:69], s[6:7], 0, v[0:1]
	v_lshlrev_b64 v[66:67], 8, v[66:67]
	v_lshl_add_u64 v[86:87], v[68:69], 0, v[66:67]
	ds_read_b128 v[66:69], v74 offset:57344
	v_add_u32_e32 v0, v88, v89
	global_load_dwordx4 v[114:117], v[86:87], off
	global_load_dwordx4 v[102:105], v[86:87], off offset:32
	global_load_dwordx4 v[90:93], v[86:87], off offset:64
	global_load_dwordx4 v[82:85], v[86:87], off offset:96
	global_load_dwordx4 v[78:81], v[86:87], off offset:128
	global_load_dwordx4 v[74:77], v[86:87], off offset:160
	s_waitcnt lgkmcnt(1)
	v_mfma_f32_32x32x16_bf16 v[2:17], v[70:73], v[62:65], v[2:17]
	ds_read_b128 v[70:73], v0 offset:49152
	global_load_dwordx4 v[106:109], v[86:87], off offset:192
	global_load_dwordx4 v[94:97], v[86:87], off offset:224
	ds_read_b128 v[138:141], v0 offset:57344
	v_lshlrev_b32_e32 v135, 2, v142
	v_or_b32_e32 v0, s22, v134
	s_waitcnt lgkmcnt(2)
	v_mfma_f32_32x32x16_bf16 v[18:33], v[66:69], v[62:65], v[18:33]
	v_add_co_u32_e32 v66, vcc, s84, v86
	s_nop 1
	v_addc_co_u32_e32 v67, vcc, 0, v87, vcc
	s_waitcnt lgkmcnt(1)
; #define LAS __attribute__((address_space(3)))
; #define FA_SBAR() __builtin_amdgcn_sched_barrier(0)
; __device__ __forceinline__ int crow(int r, int hi) { return (r & 3) + 8 * (r >> 2) + 4 * hi; }
; __device__ __forceinline__ void gla_g3(LAS unsigned char* lds, const bf16* Z, const bf16* ST, bf16* Oabc, const GlaPre pre, const float (&wa)[16], const float ba, const float* gla_norm, int item, int tid) {
;     ...
;     for (int d0 = 0; d0 < 8; ++d0) {
;         const bf16x8 a0 = *(const LAS bf16x8*)(lds + GL_KI + KSWZ256(r32, (d0 * 16 + hf * 8) * 2)), a1 = *(const LAS bf16x8*)(lds + GL_KI + KSWZ256(32 + r32, (d0 * 16 + hf * 8) * 2));
;         p0 = __builtin_amdgcn_mfma_f32_32x32x16_bf16(a0, qf[d0], p0, 0, 0, 0);
;         p1 = __builtin_amdgcn_mfma_f32_32x32x16_bf16(a1, qf[d0], p1, 0, 0, 0); }
;     { const int irow = 32 * ri + r32;
; #pragma unroll
;       for (int r = 0; r < 16; ++r) { const int j = crow(r, hf); if (j > irow) p0[r] = 0.f; if (32 + j > irow) p1[r] = 0.f; } }
;     bf16x8 pa0, pa1, pa2, pa3;
;     FA_PK4(p0, 0, pa0); FA_PK4(p0, 8, pa1); FA_PK4(p1, 0, pa2); FA_PK4(p1, 8, pa3);
;     f32x16 o[2];
; #pragma unroll
;     for (int r = 0; r < 16; ++r) { o[0][r] = 0.f; o[1][r] = 0.f; }
;     const int vb = (int)(uintptr_t)(lds + GL_V) + (cq >> 1) * 16384 + v_rd_base(lane);
; #pragma unroll
;     for (int dd = 0; dd < 2; ++dd) { const int d0v = 2 * (cq & 1) + dd;
;         s16x4 l0 = tr_read_dyn(vb + v_rd_off(d0v, 0, 0)), h0 = tr_read_dyn(vb + v_rd_off(d0v, 0, 1)), l1 = tr_read_dyn(vb + v_rd_off(d0v, 1, 0)), h1 = tr_read_dyn(vb + v_rd_off(d0v, 1, 1));
;         s16x4 l2 = tr_read_dyn(vb + v_rd_off(d0v, 2, 0)), h2 = tr_read_dyn(vb + v_rd_off(d0v, 2, 1)), l3 = tr_read_dyn(vb + v_rd_off(d0v, 3, 0)), h3 = tr_read_dyn(vb + v_rd_off(d0v, 3, 1));
;         asm volatile("s_waitcnt lgkmcnt(0)" : "+v"(l0), "+v"(h0), "+v"(l1), "+v"(h1), "+v"(l2), "+v"(h2), "+v"(l3), "+v"(h3) :: "memory"); FA_SBAR();
;         o[dd] = __builtin_amdgcn_mfma_f32_32x32x16_bf16(pa0, GL_PK(l0, h0), o[dd], 0, 0, 0);
;         o[dd] = __builtin_amdgcn_mfma_f32_32x32x16_bf16(pa1, GL_PK(l1, h1), o[dd], 0, 0, 0);
;         o[dd] = __builtin_amdgcn_mfma_f32_32x32x16_bf16(pa2, GL_PK(l2, h2), o[dd], 0, 0, 0);
;         o[dd] = __builtin_amdgcn_mfma_f32_32x32x16_bf16(pa3, GL_PK(l3, h3), o[dd], 0, 0, 0); }
	v_mfma_f32_32x32x16_bf16 v[2:17], v[70:73], v[58:61], v[2:17]
	global_load_dwordx4 v[126:129], v[66:67], off
	global_load_dwordx4 v[122:125], v[66:67], off offset:32
	global_load_dwordx4 v[118:121], v[66:67], off offset:64
	global_load_dwordx4 v[110:113], v[66:67], off offset:96
	global_load_dwordx4 v[98:101], v[66:67], off offset:128
	global_load_dwordx4 v[86:89], v[66:67], off offset:160
	global_load_dwordx4 v[70:73], v[66:67], off offset:192
	s_nop 0
	global_load_dwordx4 v[66:69], v[66:67], off offset:224
	s_waitcnt lgkmcnt(0)
	v_mfma_f32_32x32x16_bf16 v[18:33], v[138:141], v[58:61], v[18:33]
	v_or_b32_e32 v138, 32, v135
	v_cmp_le_u32_e32 vcc, v138, v0
	s_nop 9
	v_cndmask_b32_e32 v142, 0, v18, vcc
	v_cmp_le_u32_e32 vcc, v135, v0
	v_or_b32_e32 v18, 33, v135
	s_nop 0
	v_cndmask_b32_e32 v2, 0, v2, vcc
	v_cmp_lt_u32_e32 vcc, v135, v0
	s_nop 1
	v_cndmask_b32_e32 v3, 0, v3, vcc
	v_cmp_le_u32_e32 vcc, v18, v0
	v_or_b32_e32 v18, 2, v135
	s_nop 0
	v_cndmask_b32_e32 v143, 0, v19, vcc
	v_cmp_le_u32_e32 vcc, v18, v0
	v_or_b32_e32 v18, 34, v135
	s_nop 0
	v_cndmask_b32_e32 v4, 0, v4, vcc
	v_cmp_le_u32_e32 vcc, v18, v0
	v_or_b32_e32 v18, 3, v135
	s_nop 0
	v_cndmask_b32_e32 v144, 0, v20, vcc
	v_cmp_le_u32_e32 vcc, v18, v0
	v_or_b32_e32 v18, 35, v135
	s_nop 0
	v_cndmask_b32_e32 v5, 0, v5, vcc
	v_cmp_le_u32_e32 vcc, v18, v0
	v_or_b32_e32 v18, 8, v135
	s_nop 0
	v_cndmask_b32_e32 v145, 0, v21, vcc
	v_cmp_le_u32_e32 vcc, v18, v0
	v_or_b32_e32 v18, 40, v135
	s_nop 0
	v_cndmask_b32_e32 v6, 0, v6, vcc
	v_cmp_le_u32_e32 vcc, v18, v0
	v_or_b32_e32 v18, 9, v135
	s_nop 0
	v_cndmask_b32_e32 v22, 0, v22, vcc
	v_cmp_le_u32_e32 vcc, v18, v0
	v_or_b32_e32 v18, 41, v135
	s_nop 0
	v_cndmask_b32_e32 v7, 0, v7, vcc
	v_cmp_le_u32_e32 vcc, v18, v0
	v_or_b32_e32 v18, 10, v135
	s_nop 0
	v_cndmask_b32_e32 v23, 0, v23, vcc
	v_cmp_le_u32_e32 vcc, v18, v0
	v_or_b32_e32 v18, 42, v135
	s_nop 0
	v_cndmask_b32_e32 v8, 0, v8, vcc
	v_cmp_le_u32_e32 vcc, v18, v0
	v_or_b32_e32 v18, 11, v135
	s_nop 0
	v_cndmask_b32_e32 v24, 0, v24, vcc
	v_cmp_le_u32_e32 vcc, v18, v0
	v_or_b32_e32 v18, 43, v135
	s_nop 0
	v_cndmask_b32_e32 v9, 0, v9, vcc
	v_cmp_le_u32_e32 vcc, v18, v0
	v_or_b32_e32 v18, 16, v135
	s_nop 0
	v_cndmask_b32_e32 v25, 0, v25, vcc
	v_cmp_le_u32_e32 vcc, v18, v0
	v_or_b32_e32 v18, 48, v135
	s_nop 0
	v_cndmask_b32_e32 v10, 0, v10, vcc
	v_cmp_le_u32_e32 vcc, v18, v0
	v_or_b32_e32 v18, 17, v135
	s_nop 0
	v_cndmask_b32_e32 v26, 0, v26, vcc
	v_cmp_le_u32_e32 vcc, v18, v0
	v_or_b32_e32 v18, 49, v135
	s_nop 0
	v_cndmask_b32_e32 v11, 0, v11, vcc
	v_cmp_le_u32_e32 vcc, v18, v0
	v_or_b32_e32 v18, 18, v135
	s_nop 0
	v_cndmask_b32_e32 v27, 0, v27, vcc
	v_cmp_le_u32_e32 vcc, v18, v0
	v_or_b32_e32 v18, 50, v135
	s_nop 0
	v_cndmask_b32_e32 v12, 0, v12, vcc
	v_cmp_le_u32_e32 vcc, v18, v0
	v_or_b32_e32 v18, 19, v135
	s_nop 0
	v_cndmask_b32_e32 v28, 0, v28, vcc
	v_cmp_le_u32_e32 vcc, v18, v0
	v_or_b32_e32 v18, 51, v135
	s_nop 0
	v_cndmask_b32_e32 v13, 0, v13, vcc
	v_cmp_le_u32_e32 vcc, v18, v0
	v_or_b32_e32 v18, 24, v135
	s_nop 0
	v_cndmask_b32_e32 v29, 0, v29, vcc
	v_cmp_le_u32_e32 vcc, v18, v0
	v_or_b32_e32 v18, 56, v135
	s_nop 0
	v_cndmask_b32_e32 v14, 0, v14, vcc
	v_cmp_le_u32_e32 vcc, v18, v0
	v_or_b32_e32 v18, 25, v135
	s_nop 0
	v_cndmask_b32_e32 v30, 0, v30, vcc
	v_cmp_le_u32_e32 vcc, v18, v0
	v_or_b32_e32 v18, 57, v135
	s_nop 0
	v_cndmask_b32_e32 v15, 0, v15, vcc
	v_cmp_le_u32_e32 vcc, v18, v0
	v_or_b32_e32 v18, 26, v135
	s_nop 0
	v_cndmask_b32_e32 v31, 0, v31, vcc
	v_cmp_le_u32_e32 vcc, v18, v0
	v_or_b32_e32 v18, 58, v135
	s_nop 0
	v_cndmask_b32_e32 v16, 0, v16, vcc
	v_cmp_le_u32_e32 vcc, v18, v0
	v_or_b32_e32 v18, 27, v135
	s_nop 0
	v_cndmask_b32_e32 v32, 0, v32, vcc
	v_cmp_le_u32_e32 vcc, v18, v0
	v_or_b32_e32 v18, 59, v135
	s_nop 0
	v_cndmask_b32_e32 v17, 0, v17, vcc
	v_cmp_le_u32_e32 vcc, v18, v0
	v_cvt_pk_bf16_f32 v18, v2, v3
	v_cvt_pk_bf16_f32 v19, v4, v5
	v_cvt_pk_bf16_f32 v20, v6, v7
	v_cvt_pk_bf16_f32 v21, v8, v9
	v_cvt_pk_bf16_f32 v138, v10, v11
	s_nop 1
	v_cndmask_b32_e32 v0, 0, v33, vcc
	v_cvt_pk_bf16_f32 v139, v12, v13
	v_cvt_pk_bf16_f32 v140, v14, v15
	v_cvt_pk_bf16_f32 v141, v16, v17
	v_cvt_pk_bf16_f32 v142, v142, v143
	v_cvt_pk_bf16_f32 v143, v144, v145
	v_cvt_pk_bf16_f32 v144, v22, v23
	v_cvt_pk_bf16_f32 v145, v24, v25
	v_cvt_pk_bf16_f32 v146, v26, v27
	v_cvt_pk_bf16_f32 v147, v28, v29
	v_cvt_pk_bf16_f32 v148, v30, v31
	v_cvt_pk_bf16_f32 v149, v32, v0
	v_lshlrev_b32_e32 v0, 3, v150
	v_and_b32_e32 v2, 0xc0, v162
	v_lshlrev_b32_e32 v3, 1, v133
	v_and_or_b32 v2, v0, 24, v2
	v_and_b32_e32 v3, 32, v3
	v_and_b32_e32 v4, 0x100, v0
	v_or3_b32 v2, v2, v3, v4
	v_add_u32_e32 v133, s18, v2
	s_lshl_b32 s18, s20, 10
	s_and_b32 s18, s18, 0x400
	v_add_u32_e32 v150, 0x800, v133
	v_add_u32_e32 v4, s18, v133
	ds_read_b64_tr_b16 v[2:3], v4
	v_add_u32_e32 v151, 0x1000, v133
	v_add_u32_e32 v6, s18, v150
	ds_read_b64_tr_b16 v[4:5], v6
	v_add_u32_e32 v152, 0x1800, v133
	v_add_u32_e32 v6, s18, v151
	ds_read_b64_tr_b16 v[22:23], v6
	v_add_u32_e32 v154, 0x2000, v133
	v_add_u32_e32 v6, s18, v152
	ds_read_b64_tr_b16 v[24:25], v6
	v_add_u32_e32 v156, 0x2800, v133
	v_add_u32_e32 v6, s18, v154
	ds_read_b64_tr_b16 v[26:27], v6
	v_add_u32_e32 v158, 0x3000, v133
	v_add_u32_e32 v6, s18, v156
	ds_read_b64_tr_b16 v[28:29], v6
	v_add_u32_e32 v160, 0x3800, v133
	v_add_u32_e32 v6, s18, v158
	ds_read_b64_tr_b16 v[30:31], v6
	v_add_u32_e32 v6, s18, v160
	ds_read_b64_tr_b16 v[32:33], v6
	v_permlane32_swap_b32_e32 v18, v20
	s_waitcnt lgkmcnt(0)
	v_permlane32_swap_b32_e32 v19, v21
	v_permlane32_swap_b32_e32 v138, v140
	v_permlane32_swap_b32_e32 v139, v141
	v_permlane32_swap_b32_e32 v142, v144
	v_permlane32_swap_b32_e32 v143, v145
	v_permlane32_swap_b32_e32 v146, v148
	v_permlane32_swap_b32_e32 v147, v149
	v_mfma_f32_32x32x16_bf16 v[2:17], v[18:21], v[2:5], 0
	s_bitset1_b32 s18, 9
	v_mfma_f32_32x32x16_bf16 v[2:17], v[138:141], v[22:25], v[2:17]
	v_add_u32_e32 v24, s18, v133
	ds_read_b64_tr_b16 v[22:23], v24
	v_mfma_f32_32x32x16_bf16 v[2:17], v[142:145], v[26:29], v[2:17]
	v_add_u32_e32 v26, s18, v150
	ds_read_b64_tr_b16 v[24:25], v26
	v_add_u32_e32 v26, s18, v151
	ds_read_b64_tr_b16 v[150:151], v26
	v_add_u32_e32 v26, s18, v152
	ds_read_b64_tr_b16 v[152:153], v26
	v_add_u32_e32 v26, s18, v154
	ds_read_b64_tr_b16 v[154:155], v26
	v_add_u32_e32 v26, s18, v156
	ds_read_b64_tr_b16 v[156:157], v26
	v_add_u32_e32 v26, s18, v158
	ds_read_b64_tr_b16 v[158:159], v26
	v_add_u32_e32 v26, s18, v160
	ds_read_b64_tr_b16 v[160:161], v26
	v_mfma_f32_32x32x16_bf16 v[2:17], v[146:149], v[30:33], v[2:17]
	s_waitcnt lgkmcnt(0)
	s_nop 0
	v_mfma_f32_32x32x16_bf16 v[18:33], v[18:21], v[22:25], 0
	s_lshl_b32 s18, s20, 8
	s_add_i32 s18, s18, 0
	s_barrier
; #define LAS __attribute__((address_space(3)))
; __device__ __forceinline__ int crow(int r, int hi) { return (r & 3) + 8 * (r >> 2) + 4 * hi; }
; __device__ __forceinline__ void gla_g3(LAS unsigned char* lds, const bf16* Z, const bf16* ST, bf16* Oabc, const GlaPre pre, const float (&wa)[16], const float ba, const float* gla_norm, int item, int tid) {
;     ...
; #pragma unroll
;     for (int dd = 0; dd < 2; ++dd) {
; #pragma unroll
;         for (int d0 = 0; d0 < 8; ++d0) o[dd] = __builtin_amdgcn_mfma_f32_32x32x16_bf16(qf[d0], sfr[dd][d0], o[dd], 0, 0, 0); }
;     __syncthreads();
;     LAS float* Ol = (LAS float*)lds;
; #pragma unroll
;     for (int dd = 0; dd < 2; ++dd)
; #pragma unroll
;         for (int r = 0; r < 16; ++r) Ol[(32 * ri + crow(r, hf)) * 256 + 64 * cq + 32 * dd + r32] = o[dd][r];
;     __syncthreads();
;     { const f32x4 gn = *(const f32x4*)(gla_norm + h * 256 + 4 * lane);
;       v2u rw[8]; f32x4 ov[8]; float ss[8];
; #pragma unroll
;       for (int j = 0; j < 8; ++j) { const int t = wid + NWAVES * j; rw[j] = *(const v2u*)(Z + (m0 + t) * NABC + ZC_BR + h * 256 + 4 * lane); ov[j] = *(const LAS f32x4*)(Ol + t * 256 + 4 * lane); }
	v_mfma_f32_32x32x16_bf16 v[18:33], v[138:141], v[150:153], v[18:33]
	v_mfma_f32_32x32x16_bf16 v[18:33], v[142:145], v[154:157], v[18:33]
	v_mfma_f32_32x32x16_bf16 v[18:33], v[146:149], v[158:161], v[18:33]
	s_waitcnt vmcnt(15)
	v_mfma_f32_32x32x16_bf16 v[2:17], v[34:37], v[114:117], v[2:17]
	s_waitcnt vmcnt(7)
	v_mfma_f32_32x32x16_bf16 v[18:33], v[34:37], v[126:129], v[18:33]
	v_or_b32_e32 v34, s22, v135
	v_lshlrev_b32_e32 v35, 2, v134
	v_lshlrev_b32_e32 v34, 10, v34
	v_add3_u32 v34, s18, v35, v34
	s_lshl_b32 s18, s94, 2
	s_add_u32 s14, s14, s18
	s_addc_u32 s15, s15, 0
	v_mfma_f32_32x32x16_bf16 v[2:17], v[38:41], v[102:105], v[2:17]
	s_waitcnt vmcnt(6)
	v_mfma_f32_32x32x16_bf16 v[18:33], v[38:41], v[122:125], v[18:33]
	v_mfma_f32_32x32x16_bf16 v[2:17], v[42:45], v[90:93], v[2:17]
	s_waitcnt vmcnt(5)
	v_mfma_f32_32x32x16_bf16 v[18:33], v[42:45], v[118:121], v[18:33]
	v_mfma_f32_32x32x16_bf16 v[2:17], v[46:49], v[82:85], v[2:17]
	s_waitcnt vmcnt(4)
	v_mfma_f32_32x32x16_bf16 v[18:33], v[46:49], v[110:113], v[18:33]
	v_mfma_f32_32x32x16_bf16 v[2:17], v[50:53], v[78:81], v[2:17]
	s_waitcnt vmcnt(3)
	v_mfma_f32_32x32x16_bf16 v[18:33], v[50:53], v[98:101], v[18:33]
	v_mfma_f32_32x32x16_bf16 v[2:17], v[54:57], v[74:77], v[2:17]
	s_waitcnt vmcnt(2)
	v_mfma_f32_32x32x16_bf16 v[18:33], v[54:57], v[86:89], v[18:33]
	v_mfma_f32_32x32x16_bf16 v[2:17], v[62:65], v[106:109], v[2:17]
	s_waitcnt vmcnt(1)
	v_mfma_f32_32x32x16_bf16 v[18:33], v[62:65], v[70:73], v[18:33]
	v_mfma_f32_32x32x16_bf16 v[2:17], v[58:61], v[94:97], v[2:17]
	s_waitcnt vmcnt(0)
	v_mfma_f32_32x32x16_bf16 v[18:33], v[58:61], v[66:69], v[18:33]
	s_nop 11
	ds_write2_b32 v34, v2, v18 offset1:32
	v_add_u32_e32 v2, 0x400, v34
	ds_write2_b32 v2, v3, v19 offset1:32
	v_add_u32_e32 v2, 0x800, v34
	ds_write2_b32 v2, v4, v20 offset1:32
	v_add_u32_e32 v2, 0xc00, v34
	ds_write2_b32 v2, v5, v21 offset1:32
	v_add_u32_e32 v2, 0x2000, v34
	ds_write2_b32 v2, v6, v22 offset1:32
	v_add_u32_e32 v2, 0x2400, v34
	ds_write2_b32 v2, v7, v23 offset1:32
	v_add_u32_e32 v2, 0x2800, v34
	ds_write2_b32 v2, v8, v24 offset1:32
	v_add_u32_e32 v2, 0x2c00, v34
	ds_write2_b32 v2, v9, v25 offset1:32
	v_add_u32_e32 v2, 0x4000, v34
	ds_write2_b32 v2, v10, v26 offset1:32
	v_add_u32_e32 v2, 0x4400, v34
	ds_write2_b32 v2, v11, v27 offset1:32
	v_add_u32_e32 v2, 0x4800, v34
	ds_write2_b32 v2, v12, v28 offset1:32
	v_add_u32_e32 v2, 0x4c00, v34
	ds_write2_b32 v2, v13, v29 offset1:32
	v_add_u32_e32 v2, 0x6000, v34
	ds_write2_b32 v2, v14, v30 offset1:32
	v_add_u32_e32 v2, 0x6400, v34
	ds_write2_b32 v2, v15, v31 offset1:32
	v_add_u32_e32 v2, 0x6800, v34
	ds_write2_b32 v2, v16, v32 offset1:32
	v_add_u32_e32 v2, 0x6c00, v34
	ds_write2_b32 v2, v17, v33 offset1:32
	s_waitcnt lgkmcnt(0)
	s_barrier
	global_load_dwordx4 v[2:5], v162, s[14:15]
	s_ashr_i32 s14, s21, 31
	s_add_u32 s34, s4, s21
	s_addc_u32 s35, s5, s14
	s_mul_i32 s14, s35, 0x2200
	s_mul_hi_u32 s15, s34, 0x2200
	s_add_i32 s15, s15, s14
	s_mul_i32 s14, s34, 0x2200
	s_add_u32 s18, s8, s14
	s_addc_u32 s15, s9, s15
	s_lshl_b32 s14, s94, 1
	s_add_u32 s18, s18, s14
	s_addc_u32 s19, s15, 0
	s_add_i32 s15, s21, 8
	v_lshl_add_u64 v[6:7], s[18:19], 0, v[0:1]
	s_ashr_i32 s18, s15, 31
	s_add_u32 s30, s4, s15
	s_addc_u32 s31, s5, s18
	s_mul_i32 s18, s31, 0x2200
	s_mul_hi_u32 s19, s30, 0x2200
	s_add_i32 s19, s19, s18
	s_mul_i32 s18, s30, 0x2200
	s_add_u32 s18, s8, s18
	s_addc_u32 s19, s9, s19
	v_add_u32_e32 v8, 0, v162
	v_add_co_u32_e32 v6, vcc, s43, v6
	s_add_u32 s18, s18, s14
	s_nop 0
	v_addc_co_u32_e32 v7, vcc, 0, v7, vcc
	s_addc_u32 s19, s19, 0
	v_lshl_add_u32 v30, s15, 10, v8
	s_add_i32 s15, s21, 16
	global_load_dwordx2 v[44:45], v[6:7], off
	v_lshl_add_u64 v[6:7], s[18:19], 0, v[0:1]
	s_ashr_i32 s18, s15, 31
	s_add_u32 s28, s4, s15
	s_addc_u32 s29, s5, s18
	s_mul_i32 s18, s29, 0x2200
	s_mul_hi_u32 s19, s28, 0x2200
	s_add_i32 s19, s19, s18
	s_mul_i32 s18, s28, 0x2200
	s_add_u32 s18, s8, s18
	s_addc_u32 s19, s9, s19
	v_add_co_u32_e32 v6, vcc, s43, v6
	s_add_u32 s18, s18, s14
	s_nop 0
	v_addc_co_u32_e32 v7, vcc, 0, v7, vcc
	s_addc_u32 s19, s19, 0
	v_lshl_add_u32 v26, s15, 10, v8
	s_add_i32 s15, s21, 24
	global_load_dwordx2 v[52:53], v[6:7], off
	v_lshl_add_u64 v[6:7], s[18:19], 0, v[0:1]
	s_ashr_i32 s18, s15, 31
	s_add_u32 s26, s4, s15
	s_addc_u32 s27, s5, s18
	s_mul_i32 s18, s27, 0x2200
	s_mul_hi_u32 s19, s26, 0x2200
	s_add_i32 s19, s19, s18
	s_mul_i32 s18, s26, 0x2200
	s_add_u32 s18, s8, s18
	s_addc_u32 s19, s9, s19
	v_add_co_u32_e32 v6, vcc, s43, v6
	s_add_u32 s18, s18, s14
	s_nop 0
	v_addc_co_u32_e32 v7, vcc, 0, v7, vcc
	s_addc_u32 s19, s19, 0
	v_lshl_add_u32 v22, s15, 10, v8
	s_add_i32 s15, s21, 32
	global_load_dwordx2 v[50:51], v[6:7], off
	v_lshl_add_u64 v[6:7], s[18:19], 0, v[0:1]
	s_ashr_i32 s18, s15, 31
	s_add_u32 s24, s4, s15
	s_addc_u32 s25, s5, s18
	s_mul_i32 s18, s25, 0x2200
	s_mul_hi_u32 s19, s24, 0x2200
	s_add_i32 s19, s19, s18
	s_mul_i32 s18, s24, 0x2200
	s_add_u32 s18, s8, s18
	s_addc_u32 s19, s9, s19
	v_add_co_u32_e32 v6, vcc, s43, v6
	s_add_u32 s18, s18, s14
	s_nop 0
	v_addc_co_u32_e32 v7, vcc, 0, v7, vcc
	s_addc_u32 s19, s19, 0
	v_lshl_add_u32 v18, s15, 10, v8
	s_add_i32 s15, s21, 40
	global_load_dwordx2 v[48:49], v[6:7], off
	v_lshl_add_u64 v[6:7], s[18:19], 0, v[0:1]
	s_ashr_i32 s18, s15, 31
	s_add_u32 s22, s4, s15
	s_addc_u32 s23, s5, s18
	s_mul_i32 s18, s23, 0x2200
	s_mul_hi_u32 s19, s22, 0x2200
	s_add_i32 s19, s19, s18
	s_mul_i32 s18, s22, 0x2200
	s_add_u32 s18, s8, s18
	s_addc_u32 s19, s9, s19
	v_add_co_u32_e32 v6, vcc, s43, v6
	s_add_u32 s18, s18, s14
	s_nop 0
	v_addc_co_u32_e32 v7, vcc, 0, v7, vcc
	s_addc_u32 s19, s19, 0
	v_lshl_add_u32 v14, s15, 10, v8
; __device__ __forceinline__ float wave_sum(float v) { v += dpp_f<0xB1>(v); v += dpp_f<0x4E>(v); v += dpp_f<0x141>(v); v += dpp_f<0x140>(v); return sum_xor32(sum_xor16(v)); }
; #define LAS __attribute__((address_space(3)))
; __device__ __forceinline__ void gla_g3(LAS unsigned char* lds, const bf16* Z, const bf16* ST, bf16* Oabc, const GlaPre pre, const float (&wa)[16], const float ba, const float* gla_norm, int item, int tid) {
;     ...
;     { const f32x4 gn = *(const f32x4*)(gla_norm + h * 256 + 4 * lane);
;       v2u rw[8]; f32x4 ov[8]; float ss[8];
; #pragma unroll
;       for (int j = 0; j < 8; ++j) { const int t = wid + NWAVES * j; rw[j] = *(const v2u*)(Z + (m0 + t) * NABC + ZC_BR + h * 256 + 4 * lane); ov[j] = *(const LAS f32x4*)(Ol + t * 256 + 4 * lane); }
;       asm volatile("" : "+v"(ov[0]), "+v"(ov[1]), "+v"(ov[2]), "+v"(ov[3]), "+v"(ov[4]), "+v"(ov[5]), "+v"(ov[6]), "+v"(ov[7]) :: "memory");
; #pragma unroll
;       for (int j = 0; j < 8; ++j) ss[j] = (ov[j].x * ov[j].x + ov[j].y * ov[j].y) + (ov[j].z * ov[j].z + ov[j].w * ov[j].w);
; #pragma unroll
;       for (int j = 0; j < 8; ++j) ss[j] = wave_sum(ss[j]);
; #pragma unroll
;       for (int j = 0; j < 8; ++j) { const int t = wid + NWAVES * j; const float rstd = 1.0f / sqrtf(ss[j] * (1.f / 256.f) + EPS);
	s_add_i32 s15, s21, 48
	global_load_dwordx2 v[46:47], v[6:7], off
	v_lshl_add_u64 v[6:7], s[18:19], 0, v[0:1]
	s_ashr_i32 s18, s15, 31
	s_add_u32 s19, s4, s15
	s_addc_u32 s20, s5, s18
	s_mul_i32 s18, s20, 0x2200
	s_mul_hi_u32 s38, s19, 0x2200
	s_add_i32 s38, s38, s18
	s_mul_i32 s18, s19, 0x2200
	s_add_u32 s18, s8, s18
	s_addc_u32 s39, s9, s38
	s_add_u32 s38, s18, s14
	v_lshl_add_u32 v34, s21, 10, v8
	s_addc_u32 s39, s39, 0
	s_add_i32 s21, s21, 56
	s_ashr_i32 s18, s21, 31
	v_add_co_u32_e32 v6, vcc, s43, v6
	v_lshl_add_u32 v10, s15, 10, v8
	s_add_u32 s15, s4, s21
	v_addc_co_u32_e32 v7, vcc, 0, v7, vcc
	s_addc_u32 s18, s5, s18
	global_load_dwordx2 v[42:43], v[6:7], off
	v_lshl_add_u64 v[6:7], s[38:39], 0, v[0:1]
	s_mul_i32 s4, s18, 0x2200
	s_mul_hi_u32 s5, s15, 0x2200
	v_add_co_u32_e32 v6, vcc, s43, v6
	s_add_i32 s5, s5, s4
	s_mul_i32 s4, s15, 0x2200
	v_addc_co_u32_e32 v7, vcc, 0, v7, vcc
	s_add_u32 s4, s8, s4
	global_load_dwordx2 v[40:41], v[6:7], off
	s_addc_u32 s5, s9, s5
	v_lshl_add_u32 v6, s21, 10, v8
	s_add_u32 s4, s4, s14
	ds_read_b128 v[6:9], v6
	ds_read_b128 v[10:13], v10
	ds_read_b128 v[14:17], v14
	ds_read_b128 v[18:21], v18
	ds_read_b128 v[22:25], v22
	ds_read_b128 v[26:29], v26
	ds_read_b128 v[30:33], v30
	ds_read_b128 v[34:37], v34
	s_addc_u32 s5, s5, 0
	v_lshl_add_u64 v[38:39], s[4:5], 0, v[0:1]
	v_add_co_u32_e32 v38, vcc, s43, v38
	s_mov_b32 s38, 0xf800000
	s_nop 0
	v_addc_co_u32_e32 v39, vcc, 0, v39, vcc
	global_load_dwordx2 v[38:39], v[38:39], off
	s_waitcnt lgkmcnt(0)
	s_mulk_i32 s35, 0x1800
	v_mul_f32_e32 v54, v35, v35
	v_mul_f32_e32 v55, v37, v37
	v_fmac_f32_e32 v54, v34, v34
	v_fmac_f32_e32 v55, v36, v36
	v_add_f32_e32 v54, v54, v55
	v_mul_f32_e32 v55, v31, v31
	v_mul_f32_e32 v56, v33, v33
	v_fmac_f32_e32 v55, v30, v30
	v_fmac_f32_e32 v56, v32, v32
	v_add_f32_e32 v55, v55, v56
	v_mul_f32_e32 v56, v27, v27
	v_mul_f32_e32 v57, v29, v29
	v_fmac_f32_e32 v56, v26, v26
	v_fmac_f32_e32 v57, v28, v28
	v_add_f32_e32 v56, v56, v57
	v_mul_f32_e32 v57, v23, v23
	v_mul_f32_e32 v58, v25, v25
	v_fmac_f32_e32 v57, v22, v22
	v_fmac_f32_e32 v58, v24, v24
	v_add_f32_e32 v57, v57, v58
	v_mul_f32_e32 v58, v19, v19
	v_mul_f32_e32 v59, v21, v21
	v_fmac_f32_e32 v58, v18, v18
	v_fmac_f32_e32 v59, v20, v20
	v_add_f32_e32 v58, v58, v59
	v_mul_f32_e32 v59, v15, v15
	v_mul_f32_e32 v60, v17, v17
	v_fmac_f32_e32 v59, v14, v14
	v_fmac_f32_e32 v60, v16, v16
	v_add_f32_e32 v59, v59, v60
	v_mul_f32_e32 v60, v11, v11
	v_mul_f32_e32 v61, v13, v13
	v_add_f32_dpp v54, v54, v54 quad_perm:[1,0,3,2] row_mask:0xf bank_mask:0xf bound_ctrl:1
	v_fmac_f32_e32 v60, v10, v10
	v_fmac_f32_e32 v61, v12, v12
	v_add_f32_dpp v54, v54, v54 quad_perm:[2,3,0,1] row_mask:0xf bank_mask:0xf bound_ctrl:1
	v_add_f32_e32 v60, v60, v61
	v_mul_f32_e32 v61, v7, v7
	v_mul_f32_e32 v62, v9, v9
	v_add_f32_dpp v54, v54, v54 row_half_mirror row_mask:0xf bank_mask:0xf bound_ctrl:1
	v_fmac_f32_e32 v61, v6, v6
	v_fmac_f32_e32 v62, v8, v8
	v_add_f32_dpp v54, v54, v54 row_mirror row_mask:0xf bank_mask:0xf bound_ctrl:1
	v_add_f32_e32 v61, v61, v62
	v_mov_b32_e32 v62, v54
	s_nop 1
	v_permlane16_swap_b32_e32 v54, v62
	v_add_f32_dpp v55, v55, v55 quad_perm:[1,0,3,2] row_mask:0xf bank_mask:0xf bound_ctrl:1
	v_add_f32_e32 v54, v54, v62
	v_mov_b32_e32 v62, v54
	v_add_f32_dpp v55, v55, v55 quad_perm:[2,3,0,1] row_mask:0xf bank_mask:0xf bound_ctrl:1
	s_nop 0
	v_permlane32_swap_b32_e32 v54, v62
	v_add_f32_dpp v55, v55, v55 row_half_mirror row_mask:0xf bank_mask:0xf bound_ctrl:1
	v_add_f32_e32 v54, v54, v62
	v_fmamk_f32 v54, v54, 0x3b800000, v225
	v_add_f32_dpp v55, v55, v55 row_mirror row_mask:0xf bank_mask:0xf bound_ctrl:1
	v_mov_b32_e32 v62, v55
	s_nop 1
	v_permlane16_swap_b32_e32 v55, v62
	v_add_f32_e32 v55, v55, v62
	v_mov_b32_e32 v62, v55
	s_nop 1
	v_permlane32_swap_b32_e32 v55, v62
	v_add_f32_e32 v70, v55, v62
	s_nop 0
	v_add_f32_dpp v55, v56, v56 quad_perm:[1,0,3,2] row_mask:0xf bank_mask:0xf bound_ctrl:1
	v_cmp_gt_f32_e32 vcc, s38, v54
	s_mulk_i32 s31, 0x1800
	v_add_f32_dpp v55, v55, v55 quad_perm:[2,3,0,1] row_mask:0xf bank_mask:0xf bound_ctrl:1
	s_mulk_i32 s29, 0x1800
	s_mulk_i32 s27, 0x1800
	v_add_f32_dpp v55, v55, v55 row_half_mirror row_mask:0xf bank_mask:0xf bound_ctrl:1
	s_mulk_i32 s25, 0x1800
	s_mulk_i32 s23, 0x1800
	v_add_f32_dpp v55, v55, v55 row_mirror row_mask:0xf bank_mask:0xf bound_ctrl:1
	v_mov_b32_e32 v56, v55
	s_nop 1
	v_permlane16_swap_b32_e32 v55, v56
	v_add_f32_e32 v55, v55, v56
	v_mov_b32_e32 v56, v55
	s_nop 1
	v_permlane32_swap_b32_e32 v55, v56
	v_add_f32_e32 v71, v55, v56
	s_nop 0
	v_add_f32_dpp v55, v57, v57 quad_perm:[1,0,3,2] row_mask:0xf bank_mask:0xf bound_ctrl:1
	s_mulk_i32 s20, 0x1800
	s_mulk_i32 s18, 0x1800
	v_add_f32_dpp v55, v55, v55 quad_perm:[2,3,0,1] row_mask:0xf bank_mask:0xf bound_ctrl:1
	s_nop 1
	v_add_f32_dpp v55, v55, v55 row_half_mirror row_mask:0xf bank_mask:0xf bound_ctrl:1
	s_nop 1
	v_add_f32_dpp v55, v55, v55 row_mirror row_mask:0xf bank_mask:0xf bound_ctrl:1
	v_mov_b32_e32 v56, v55
	s_nop 1
	v_permlane16_swap_b32_e32 v55, v56
	v_add_f32_e32 v55, v55, v56
	v_mov_b32_e32 v56, v55
	s_nop 1
	v_permlane32_swap_b32_e32 v55, v56
	v_add_f32_e32 v72, v55, v56
	s_nop 0
	v_add_f32_dpp v55, v58, v58 quad_perm:[1,0,3,2] row_mask:0xf bank_mask:0xf bound_ctrl:1
	s_nop 1
	v_add_f32_dpp v55, v55, v55 quad_perm:[2,3,0,1] row_mask:0xf bank_mask:0xf bound_ctrl:1
	s_nop 1
	v_add_f32_dpp v55, v55, v55 row_half_mirror row_mask:0xf bank_mask:0xf bound_ctrl:1
	s_nop 1
	v_add_f32_dpp v55, v55, v55 row_mirror row_mask:0xf bank_mask:0xf bound_ctrl:1
	v_mov_b32_e32 v56, v55
	s_nop 1
	v_permlane16_swap_b32_e32 v55, v56
	v_add_f32_e32 v55, v55, v56
	v_mov_b32_e32 v56, v55
	s_nop 1
; __device__ __forceinline__ unsigned pk2(float lo, float hi) { return f2bf(lo) | (f2bf(hi) << 16); }
; __device__ __forceinline__ float bflo(unsigned w) { return __uint_as_float(w << 16); }
; __device__ __forceinline__ float bfhi(unsigned w) { return __uint_as_float(w & 0xffff0000u); }
; __device__ __forceinline__ void gla_g3(LAS unsigned char* lds, const bf16* Z, const bf16* ST, bf16* Oabc, const GlaPre pre, const float (&wa)[16], const float ba, const float* gla_norm, int item, int tid) {
;     ...
;       for (int j = 0; j < 8; ++j) { const int t = wid + NWAVES * j; const float rstd = 1.0f / sqrtf(ss[j] * (1.f / 256.f) + EPS);
;           const float r0 = bflo(rw[j].x), r1 = bfhi(rw[j].x), r2 = bflo(rw[j].y), r3 = bfhi(rw[j].y);
;           v2u w; w.x = pk2(ov[j].x * rstd * gn.x * (r0 * __builtin_amdgcn_rcpf(1.0f + __expf(-r0))), ov[j].y * rstd * gn.y * (r1 * __builtin_amdgcn_rcpf(1.0f + __expf(-r1))));
;           w.y = pk2(ov[j].z * rstd * gn.z * (r2 * __builtin_amdgcn_rcpf(1.0f + __expf(-r2))), ov[j].w * rstd * gn.w * (r3 * __builtin_amdgcn_rcpf(1.0f + __expf(-r3))));
;           *(v2u*)(Oabc + (m0 + t) * 3072 + 1024 + h * 256 + 4 * lane) = w; } }
	v_permlane32_swap_b32_e32 v55, v56
	v_add_f32_e32 v57, v55, v56
	s_nop 0
	v_add_f32_dpp v55, v59, v59 quad_perm:[1,0,3,2] row_mask:0xf bank_mask:0xf bound_ctrl:1
	s_nop 1
	v_add_f32_dpp v55, v55, v55 quad_perm:[2,3,0,1] row_mask:0xf bank_mask:0xf bound_ctrl:1
	s_nop 1
	v_add_f32_dpp v55, v55, v55 row_half_mirror row_mask:0xf bank_mask:0xf bound_ctrl:1
	s_nop 1
	v_add_f32_dpp v55, v55, v55 row_mirror row_mask:0xf bank_mask:0xf bound_ctrl:1
	v_mov_b32_e32 v56, v55
	s_nop 1
	v_permlane16_swap_b32_e32 v55, v56
	v_add_f32_e32 v55, v55, v56
	v_mov_b32_e32 v56, v55
	s_nop 1
	v_permlane32_swap_b32_e32 v55, v56
	v_add_f32_e32 v56, v55, v56
	s_nop 0
	v_add_f32_dpp v55, v60, v60 quad_perm:[1,0,3,2] row_mask:0xf bank_mask:0xf bound_ctrl:1
	v_mul_f32_e32 v60, 0x4f800000, v54
	v_cndmask_b32_e32 v54, v54, v60, vcc
	v_add_f32_dpp v55, v55, v55 quad_perm:[2,3,0,1] row_mask:0xf bank_mask:0xf bound_ctrl:1
	v_sqrt_f32_e32 v60, v54
	s_nop 0
	v_add_f32_dpp v55, v55, v55 row_half_mirror row_mask:0xf bank_mask:0xf bound_ctrl:1
	s_nop 1
	v_add_f32_dpp v55, v55, v55 row_mirror row_mask:0xf bank_mask:0xf bound_ctrl:1
	v_mov_b32_e32 v58, v55
	s_nop 1
	v_permlane16_swap_b32_e32 v55, v58
	v_add_f32_e32 v55, v55, v58
	v_mov_b32_e32 v58, v55
	s_nop 1
	v_permlane32_swap_b32_e32 v55, v58
	v_add_f32_e32 v55, v55, v58
	s_nop 0
	v_add_f32_dpp v58, v61, v61 quad_perm:[1,0,3,2] row_mask:0xf bank_mask:0xf bound_ctrl:1
	v_add_u32_e32 v61, -1, v60
	v_fma_f32 v62, -v61, v60, v54
	v_cmp_ge_f32_e64 s[4:5], 0, v62
	v_add_u32_e32 v62, 1, v60
	v_add_f32_dpp v58, v58, v58 quad_perm:[2,3,0,1] row_mask:0xf bank_mask:0xf bound_ctrl:1
	v_cndmask_b32_e64 v61, v60, v61, s[4:5]
	v_fma_f32 v60, -v62, v60, v54
	v_cmp_lt_f32_e64 s[4:5], 0, v60
	v_add_f32_dpp v58, v58, v58 row_half_mirror row_mask:0xf bank_mask:0xf bound_ctrl:1
	s_nop 0
	v_cndmask_b32_e64 v60, v61, v62, s[4:5]
	v_mul_f32_e32 v61, 0x37800000, v60
	v_cndmask_b32_e32 v60, v60, v61, vcc
	v_cmp_class_f32_e32 vcc, v54, v222
	v_add_f32_dpp v58, v58, v58 row_mirror row_mask:0xf bank_mask:0xf bound_ctrl:1
	v_mov_b32_e32 v59, v58
	v_cndmask_b32_e32 v60, v60, v54, vcc
	v_div_scale_f32 v61, s[4:5], v60, v60, 1.0
	v_permlane16_swap_b32_e32 v58, v59
	v_rcp_f32_e32 v62, v61
	v_add_f32_e32 v58, v58, v59
	v_mov_b32_e32 v59, v58
	s_nop 1
	v_permlane32_swap_b32_e32 v58, v59
	v_add_f32_e32 v54, v58, v59
	v_fma_f32 v58, -v61, v62, 1.0
	v_fmac_f32_e32 v62, v58, v62
	v_div_scale_f32 v58, vcc, 1.0, v60, 1.0
	v_mul_f32_e32 v59, v58, v62
	v_fma_f32 v63, -v61, v59, v58
	v_fmac_f32_e32 v59, v63, v62
	v_fma_f32 v58, -v61, v59, v58
	v_div_fmas_f32 v58, v58, v62, v59
	v_div_fixup_f32 v58, v58, v60, 1.0
	s_waitcnt vmcnt(7)
	v_lshlrev_b32_e32 v60, 16, v44
	v_and_b32_e32 v62, 0xffff0000, v44
	v_mul_f32_e32 v44, 0xbfb8aa3b, v60
	v_exp_f32_e32 v44, v44
	v_mul_f32_e32 v59, 0xbfb8aa3b, v62
	v_exp_f32_e32 v59, v59
	v_lshlrev_b32_e32 v61, 16, v45
	v_add_f32_e32 v44, 1.0, v44
	v_rcp_f32_e32 v64, v44
	v_add_f32_e32 v44, 1.0, v59
	v_rcp_f32_e32 v66, v44
	v_mov_b32_e32 v44, v34
	v_mul_f32_e32 v34, 0xbfb8aa3b, v61
	v_exp_f32_e32 v34, v34
	v_and_b32_e32 v63, 0xffff0000, v45
	v_mov_b32_e32 v45, v36
	v_pk_mul_f32 v[68:69], v[44:45], v[58:59] op_sel_hi:[1,0]
	v_mov_b32_e32 v44, v2
	v_add_f32_e32 v2, 1.0, v34
	v_rcp_f32_e32 v65, v2
	v_mul_f32_e32 v2, 0xbfb8aa3b, v63
	v_exp_f32_e32 v2, v2
	v_mov_b32_e32 v36, v35
	v_mov_b32_e32 v45, v4
	v_pk_mul_f32 v[34:35], v[36:37], v[58:59] op_sel_hi:[1,0]
	v_add_f32_e32 v2, 1.0, v2
	v_rcp_f32_e32 v67, v2
	v_mov_b32_e32 v4, v3
	v_pk_mul_f32 v[2:3], v[4:5], v[34:35]
	v_pk_mul_f32 v[68:69], v[44:45], v[68:69]
	v_pk_mul_f32 v[34:35], v[66:67], v[62:63]
	v_pk_mul_f32 v[60:61], v[64:65], v[60:61]
	v_pk_mul_f32 v[2:3], v[34:35], v[2:3]
	v_pk_mul_f32 v[60:61], v[60:61], v[68:69]
	v_and_b32_sdwa v36, v3, v224 dst_sel:DWORD dst_unused:UNUSED_PAD src0_sel:WORD_1 src1_sel:DWORD
	v_and_b32_sdwa v34, v61, v224 dst_sel:DWORD dst_unused:UNUSED_PAD src0_sel:WORD_1 src1_sel:DWORD
	v_and_b32_sdwa v37, v2, v224 dst_sel:DWORD dst_unused:UNUSED_PAD src0_sel:WORD_1 src1_sel:DWORD
	v_add3_u32 v3, v3, v36, s40
	v_and_b32_sdwa v35, v60, v224 dst_sel:DWORD dst_unused:UNUSED_PAD src0_sel:WORD_1 src1_sel:DWORD
	v_add3_u32 v34, v61, v34, s40
	v_add3_u32 v2, v2, v37, s40
	v_and_b32_e32 v3, 0xffff0000, v3
	v_add3_u32 v35, v60, v35, s40
	v_and_b32_e32 v2, 0xffff0000, v2
	v_or_b32_sdwa v3, v3, v34 dst_sel:DWORD dst_unused:UNUSED_PAD src0_sel:DWORD src1_sel:WORD_1
	v_fmamk_f32 v34, v70, 0x3b800000, v225
	v_or_b32_sdwa v2, v2, v35 dst_sel:DWORD dst_unused:UNUSED_PAD src0_sel:DWORD src1_sel:WORD_1
	v_mul_f32_e32 v35, 0x4f800000, v34
	v_cmp_gt_f32_e32 vcc, s38, v34
	s_mul_hi_u32 s4, s34, 0x1800
	s_add_i32 s4, s4, s35
	v_cndmask_b32_e32 v34, v34, v35, vcc
	v_sqrt_f32_e32 v35, v34
	s_mulk_i32 s34, 0x1800
	s_add_u32 s21, s0, s34
	s_addc_u32 s34, s1, s4
	v_add_u32_e32 v36, -1, v35
	v_fma_f32 v37, -v36, v35, v34
	v_cmp_ge_f32_e64 s[4:5], 0, v37
	v_add_u32_e32 v37, 1, v35
	v_mov_b32_e32 v60, v30
	v_cndmask_b32_e64 v36, v35, v36, s[4:5]
	v_fma_f32 v35, -v37, v35, v34
	v_cmp_lt_f32_e64 s[4:5], 0, v35
	v_mov_b32_e32 v61, v32
	v_mov_b32_e32 v32, v31
	v_cndmask_b32_e64 v35, v36, v37, s[4:5]
	v_mul_f32_e32 v36, 0x37800000, v35
	v_cndmask_b32_e32 v35, v35, v36, vcc
	v_cmp_class_f32_e32 vcc, v34, v222
	s_nop 1
	v_cndmask_b32_e32 v34, v35, v34, vcc
	v_div_scale_f32 v35, s[4:5], v34, v34, 1.0
	v_rcp_f32_e32 v36, v35
	s_add_u32 s4, s21, s14
	s_addc_u32 s5, s34, 0
	s_nop 1
	global_store_dwordx2 v0, v[2:3], s[4:5] offset:2048
	v_fma_f32 v2, -v35, v36, 1.0
	v_fmac_f32_e32 v36, v2, v36
	v_div_scale_f32 v2, vcc, 1.0, v34, 1.0
	v_mul_f32_e32 v3, v2, v36
	v_fma_f32 v37, -v35, v3, v2
	v_fmac_f32_e32 v3, v37, v36
	v_fma_f32 v2, -v35, v3, v2
	v_div_fmas_f32 v2, v2, v36, v3
	v_div_fixup_f32 v2, v2, v34, 1.0
	s_waitcnt vmcnt(7)
; __device__ __forceinline__ unsigned pk2(float lo, float hi) { return f2bf(lo) | (f2bf(hi) << 16); }
; __device__ __forceinline__ float bflo(unsigned w) { return __uint_as_float(w << 16); }
; __device__ __forceinline__ float bfhi(unsigned w) { return __uint_as_float(w & 0xffff0000u); }
; __device__ __forceinline__ void gla_g3(LAS unsigned char* lds, const bf16* Z, const bf16* ST, bf16* Oabc, const GlaPre pre, const float (&wa)[16], const float ba, const float* gla_norm, int item, int tid) {
;     ...
;       for (int j = 0; j < 8; ++j) { const int t = wid + NWAVES * j; const float rstd = 1.0f / sqrtf(ss[j] * (1.f / 256.f) + EPS);
;           const float r0 = bflo(rw[j].x), r1 = bfhi(rw[j].x), r2 = bflo(rw[j].y), r3 = bfhi(rw[j].y);
;           v2u w; w.x = pk2(ov[j].x * rstd * gn.x * (r0 * __builtin_amdgcn_rcpf(1.0f + __expf(-r0))), ov[j].y * rstd * gn.y * (r1 * __builtin_amdgcn_rcpf(1.0f + __expf(-r1))));
;           w.y = pk2(ov[j].z * rstd * gn.z * (r2 * __builtin_amdgcn_rcpf(1.0f + __expf(-r2))), ov[j].w * rstd * gn.w * (r3 * __builtin_amdgcn_rcpf(1.0f + __expf(-r3))));
;           *(v2u*)(Oabc + (m0 + t) * 3072 + 1024 + h * 256 + 4 * lane) = w; } }
	v_lshlrev_b32_e32 v34, 16, v52
	v_and_b32_e32 v36, 0xffff0000, v52
	v_mul_f32_e32 v3, 0xbfb8aa3b, v34
	v_exp_f32_e32 v3, v3
	v_mul_f32_e32 v37, 0xbfb8aa3b, v36
	v_exp_f32_e32 v58, v37
	v_lshlrev_b32_e32 v35, 16, v53
	v_add_f32_e32 v3, 1.0, v3
	v_rcp_f32_e32 v52, v3
	v_add_f32_e32 v3, 1.0, v58
	v_rcp_f32_e32 v58, v3
	v_mul_f32_e32 v3, 0xbfb8aa3b, v35
	v_exp_f32_e32 v3, v3
	v_and_b32_e32 v37, 0xffff0000, v53
	s_mul_hi_u32 s4, s30, 0x1800
	s_add_i32 s4, s4, s31
	v_pk_mul_f32 v[60:61], v[60:61], v[2:3] op_sel_hi:[1,0]
	v_add_f32_e32 v3, 1.0, v3
	v_rcp_f32_e32 v53, v3
	v_mul_f32_e32 v3, 0xbfb8aa3b, v37
	v_exp_f32_e32 v3, v3
	v_pk_mul_f32 v[60:61], v[44:45], v[60:61]
	v_pk_mul_f32 v[34:35], v[52:53], v[34:35]
	s_mulk_i32 s30, 0x1800
	v_add_f32_e32 v3, 1.0, v3
	v_rcp_f32_e32 v59, v3
	v_pk_mul_f32 v[2:3], v[32:33], v[2:3] op_sel_hi:[1,0]
	v_pk_mul_f32 v[34:35], v[34:35], v[60:61]
	v_pk_mul_f32 v[2:3], v[4:5], v[2:3]
	v_pk_mul_f32 v[30:31], v[58:59], v[36:37]
	s_add_u32 s21, s0, s30
	v_pk_mul_f32 v[2:3], v[30:31], v[2:3]
	v_and_b32_sdwa v30, v35, v224 dst_sel:DWORD dst_unused:UNUSED_PAD src0_sel:WORD_1 src1_sel:DWORD
	v_and_b32_sdwa v32, v3, v224 dst_sel:DWORD dst_unused:UNUSED_PAD src0_sel:WORD_1 src1_sel:DWORD
	v_and_b32_sdwa v33, v2, v224 dst_sel:DWORD dst_unused:UNUSED_PAD src0_sel:WORD_1 src1_sel:DWORD
	v_add3_u32 v3, v3, v32, s40
	v_and_b32_sdwa v31, v34, v224 dst_sel:DWORD dst_unused:UNUSED_PAD src0_sel:WORD_1 src1_sel:DWORD
	v_add3_u32 v30, v35, v30, s40
	v_add3_u32 v2, v2, v33, s40
	v_and_b32_e32 v3, 0xffff0000, v3
	v_add3_u32 v31, v34, v31, s40
	v_and_b32_e32 v2, 0xffff0000, v2
	v_or_b32_sdwa v3, v3, v30 dst_sel:DWORD dst_unused:UNUSED_PAD src0_sel:DWORD src1_sel:WORD_1
	v_fmamk_f32 v30, v71, 0x3b800000, v225
	v_or_b32_sdwa v2, v2, v31 dst_sel:DWORD dst_unused:UNUSED_PAD src0_sel:DWORD src1_sel:WORD_1
	v_mul_f32_e32 v31, 0x4f800000, v30
	v_cmp_gt_f32_e32 vcc, s38, v30
	s_addc_u32 s30, s1, s4
	s_nop 0
	v_cndmask_b32_e32 v30, v30, v31, vcc
	v_sqrt_f32_e32 v31, v30
	s_nop 0
	v_add_u32_e32 v32, -1, v31
	v_fma_f32 v33, -v32, v31, v30
	v_cmp_ge_f32_e64 s[4:5], 0, v33
	v_add_u32_e32 v33, 1, v31
	s_nop 0
	v_cndmask_b32_e64 v32, v31, v32, s[4:5]
	v_fma_f32 v31, -v33, v31, v30
	v_cmp_lt_f32_e64 s[4:5], 0, v31
	s_nop 1
	v_cndmask_b32_e64 v31, v32, v33, s[4:5]
	v_mul_f32_e32 v32, 0x37800000, v31
	v_cndmask_b32_e32 v31, v31, v32, vcc
	v_cmp_class_f32_e32 vcc, v30, v222
	s_nop 1
	v_cndmask_b32_e32 v30, v31, v30, vcc
	v_div_scale_f32 v31, s[4:5], v30, v30, 1.0
	v_rcp_f32_e32 v32, v31
	s_add_u32 s4, s21, s14
	s_addc_u32 s5, s30, 0
	s_nop 1
	global_store_dwordx2 v0, v[2:3], s[4:5] offset:2048
	v_fma_f32 v2, -v31, v32, 1.0
	v_fmac_f32_e32 v32, v2, v32
	v_div_scale_f32 v2, vcc, 1.0, v30, 1.0
	v_mul_f32_e32 v3, v2, v32
	v_fma_f32 v33, -v31, v3, v2
	v_fmac_f32_e32 v3, v33, v32
	v_fma_f32 v2, -v31, v3, v2
	v_div_fmas_f32 v2, v2, v32, v3
	v_div_fixup_f32 v2, v2, v30, 1.0
	s_waitcnt vmcnt(7)
	v_lshlrev_b32_e32 v30, 16, v50
	v_and_b32_e32 v32, 0xffff0000, v50
	v_mul_f32_e32 v3, 0xbfb8aa3b, v30
	v_exp_f32_e32 v3, v3
	v_mul_f32_e32 v33, 0xbfb8aa3b, v32
	v_exp_f32_e32 v35, v33
	v_lshlrev_b32_e32 v31, 16, v51
	v_add_f32_e32 v3, 1.0, v3
	v_rcp_f32_e32 v34, v3
	v_add_f32_e32 v3, 1.0, v35
	v_rcp_f32_e32 v36, v3
	v_mul_f32_e32 v3, 0xbfb8aa3b, v31
	v_exp_f32_e32 v3, v3
	v_and_b32_e32 v33, 0xffff0000, v51
	v_mov_b32_e32 v50, v26
	v_mov_b32_e32 v51, v28
	v_pk_mul_f32 v[50:51], v[50:51], v[2:3] op_sel_hi:[1,0]
	v_add_f32_e32 v3, 1.0, v3
	v_rcp_f32_e32 v35, v3
	v_mul_f32_e32 v3, 0xbfb8aa3b, v33
	v_exp_f32_e32 v3, v3
	v_mov_b32_e32 v28, v27
	v_pk_mul_f32 v[50:51], v[44:45], v[50:51]
	v_pk_mul_f32 v[30:31], v[34:35], v[30:31]
	v_add_f32_e32 v3, 1.0, v3
	v_rcp_f32_e32 v37, v3
	v_pk_mul_f32 v[2:3], v[28:29], v[2:3] op_sel_hi:[1,0]
	v_pk_mul_f32 v[30:31], v[30:31], v[50:51]
	v_pk_mul_f32 v[2:3], v[4:5], v[2:3]
	v_pk_mul_f32 v[26:27], v[36:37], v[32:33]
	s_mul_hi_u32 s4, s28, 0x1800
	v_pk_mul_f32 v[2:3], v[26:27], v[2:3]
	v_and_b32_sdwa v26, v31, v224 dst_sel:DWORD dst_unused:UNUSED_PAD src0_sel:WORD_1 src1_sel:DWORD
	v_and_b32_sdwa v28, v3, v224 dst_sel:DWORD dst_unused:UNUSED_PAD src0_sel:WORD_1 src1_sel:DWORD
	v_and_b32_sdwa v29, v2, v224 dst_sel:DWORD dst_unused:UNUSED_PAD src0_sel:WORD_1 src1_sel:DWORD
	v_add3_u32 v3, v3, v28, s40
	v_and_b32_sdwa v27, v30, v224 dst_sel:DWORD dst_unused:UNUSED_PAD src0_sel:WORD_1 src1_sel:DWORD
	v_add3_u32 v26, v31, v26, s40
	v_add3_u32 v2, v2, v29, s40
	v_and_b32_e32 v3, 0xffff0000, v3
	v_add3_u32 v27, v30, v27, s40
	v_and_b32_e32 v2, 0xffff0000, v2
	v_or_b32_sdwa v3, v3, v26 dst_sel:DWORD dst_unused:UNUSED_PAD src0_sel:DWORD src1_sel:WORD_1
	v_fmamk_f32 v26, v72, 0x3b800000, v225
	v_or_b32_sdwa v2, v2, v27 dst_sel:DWORD dst_unused:UNUSED_PAD src0_sel:DWORD src1_sel:WORD_1
	v_mul_f32_e32 v27, 0x4f800000, v26
	v_cmp_gt_f32_e32 vcc, s38, v26
	s_add_i32 s4, s4, s29
	s_mulk_i32 s28, 0x1800
	v_cndmask_b32_e32 v26, v26, v27, vcc
	v_sqrt_f32_e32 v27, v26
	s_add_u32 s21, s0, s28
	s_addc_u32 s28, s1, s4
	v_mov_b32_e32 v34, v22
	v_add_u32_e32 v28, -1, v27
	v_fma_f32 v29, -v28, v27, v26
	v_cmp_ge_f32_e64 s[4:5], 0, v29
	v_add_u32_e32 v29, 1, v27
	v_mov_b32_e32 v35, v24
	v_cndmask_b32_e64 v28, v27, v28, s[4:5]
	v_fma_f32 v27, -v29, v27, v26
	v_cmp_lt_f32_e64 s[4:5], 0, v27
	v_mov_b32_e32 v24, v23
	s_nop 0
	v_cndmask_b32_e64 v27, v28, v29, s[4:5]
	v_mul_f32_e32 v28, 0x37800000, v27
	v_cndmask_b32_e32 v27, v27, v28, vcc
	v_cmp_class_f32_e32 vcc, v26, v222
	s_nop 1
	v_cndmask_b32_e32 v26, v27, v26, vcc
	v_div_scale_f32 v27, s[4:5], v26, v26, 1.0
	v_rcp_f32_e32 v28, v27
	s_add_u32 s4, s21, s14
	s_addc_u32 s5, s28, 0
	s_nop 1
	global_store_dwordx2 v0, v[2:3], s[4:5] offset:2048
	v_fma_f32 v2, -v27, v28, 1.0
	v_fmac_f32_e32 v28, v2, v28
	v_div_scale_f32 v2, vcc, 1.0, v26, 1.0
	v_mul_f32_e32 v3, v2, v28
	v_fma_f32 v29, -v27, v3, v2
	v_fmac_f32_e32 v3, v29, v28
	v_fma_f32 v2, -v27, v3, v2
	v_div_fmas_f32 v2, v2, v28, v3
	v_div_fixup_f32 v2, v2, v26, 1.0
	s_waitcnt vmcnt(7)
; __device__ __forceinline__ unsigned pk2(float lo, float hi) { return f2bf(lo) | (f2bf(hi) << 16); }
; __device__ __forceinline__ float bflo(unsigned w) { return __uint_as_float(w << 16); }
; __device__ __forceinline__ float bfhi(unsigned w) { return __uint_as_float(w & 0xffff0000u); }
; __device__ __forceinline__ void gla_g3(LAS unsigned char* lds, const bf16* Z, const bf16* ST, bf16* Oabc, const GlaPre pre, const float (&wa)[16], const float ba, const float* gla_norm, int item, int tid) {
;     ...
;       for (int j = 0; j < 8; ++j) { const int t = wid + NWAVES * j; const float rstd = 1.0f / sqrtf(ss[j] * (1.f / 256.f) + EPS);
;           const float r0 = bflo(rw[j].x), r1 = bfhi(rw[j].x), r2 = bflo(rw[j].y), r3 = bfhi(rw[j].y);
;           v2u w; w.x = pk2(ov[j].x * rstd * gn.x * (r0 * __builtin_amdgcn_rcpf(1.0f + __expf(-r0))), ov[j].y * rstd * gn.y * (r1 * __builtin_amdgcn_rcpf(1.0f + __expf(-r1))));
;           w.y = pk2(ov[j].z * rstd * gn.z * (r2 * __builtin_amdgcn_rcpf(1.0f + __expf(-r2))), ov[j].w * rstd * gn.w * (r3 * __builtin_amdgcn_rcpf(1.0f + __expf(-r3))));
;           *(v2u*)(Oabc + (m0 + t) * 3072 + 1024 + h * 256 + 4 * lane) = w; } }
	v_lshlrev_b32_e32 v26, 16, v48
	v_and_b32_e32 v28, 0xffff0000, v48
	v_mul_f32_e32 v3, 0xbfb8aa3b, v26
	v_exp_f32_e32 v3, v3
	v_mul_f32_e32 v29, 0xbfb8aa3b, v28
	v_exp_f32_e32 v31, v29
	v_lshlrev_b32_e32 v27, 16, v49
	v_add_f32_e32 v3, 1.0, v3
	v_rcp_f32_e32 v30, v3
	v_add_f32_e32 v3, 1.0, v31
	v_rcp_f32_e32 v32, v3
	v_mul_f32_e32 v3, 0xbfb8aa3b, v27
	v_exp_f32_e32 v3, v3
	v_and_b32_e32 v29, 0xffff0000, v49
	s_mul_hi_u32 s4, s26, 0x1800
	s_add_i32 s4, s4, s27
	v_pk_mul_f32 v[34:35], v[34:35], v[2:3] op_sel_hi:[1,0]
	v_add_f32_e32 v3, 1.0, v3
	v_rcp_f32_e32 v31, v3
	v_mul_f32_e32 v3, 0xbfb8aa3b, v29
	v_exp_f32_e32 v3, v3
	v_pk_mul_f32 v[34:35], v[44:45], v[34:35]
	v_pk_mul_f32 v[26:27], v[30:31], v[26:27]
	s_mulk_i32 s26, 0x1800
	v_add_f32_e32 v3, 1.0, v3
	v_rcp_f32_e32 v33, v3
	v_pk_mul_f32 v[2:3], v[24:25], v[2:3] op_sel_hi:[1,0]
	v_pk_mul_f32 v[26:27], v[26:27], v[34:35]
	v_pk_mul_f32 v[2:3], v[4:5], v[2:3]
	v_pk_mul_f32 v[22:23], v[32:33], v[28:29]
	s_add_u32 s21, s0, s26
	v_pk_mul_f32 v[2:3], v[22:23], v[2:3]
	v_and_b32_sdwa v22, v27, v224 dst_sel:DWORD dst_unused:UNUSED_PAD src0_sel:WORD_1 src1_sel:DWORD
	v_and_b32_sdwa v24, v3, v224 dst_sel:DWORD dst_unused:UNUSED_PAD src0_sel:WORD_1 src1_sel:DWORD
	v_and_b32_sdwa v25, v2, v224 dst_sel:DWORD dst_unused:UNUSED_PAD src0_sel:WORD_1 src1_sel:DWORD
	v_add3_u32 v3, v3, v24, s40
	v_and_b32_sdwa v23, v26, v224 dst_sel:DWORD dst_unused:UNUSED_PAD src0_sel:WORD_1 src1_sel:DWORD
	v_add3_u32 v22, v27, v22, s40
	v_add3_u32 v2, v2, v25, s40
	v_and_b32_e32 v3, 0xffff0000, v3
	v_add3_u32 v23, v26, v23, s40
	v_and_b32_e32 v2, 0xffff0000, v2
	v_or_b32_sdwa v3, v3, v22 dst_sel:DWORD dst_unused:UNUSED_PAD src0_sel:DWORD src1_sel:WORD_1
	v_fmamk_f32 v22, v57, 0x3b800000, v225
	v_or_b32_sdwa v2, v2, v23 dst_sel:DWORD dst_unused:UNUSED_PAD src0_sel:DWORD src1_sel:WORD_1
	v_mul_f32_e32 v23, 0x4f800000, v22
	v_cmp_gt_f32_e32 vcc, s38, v22
	s_addc_u32 s26, s1, s4
	v_mov_b32_e32 v30, v18
	v_cndmask_b32_e32 v22, v22, v23, vcc
	v_sqrt_f32_e32 v23, v22
	v_mov_b32_e32 v31, v20
	v_mov_b32_e32 v20, v19
	v_add_u32_e32 v24, -1, v23
	v_fma_f32 v25, -v24, v23, v22
	v_cmp_ge_f32_e64 s[4:5], 0, v25
	v_add_u32_e32 v25, 1, v23
	s_nop 0
	v_cndmask_b32_e64 v24, v23, v24, s[4:5]
	v_fma_f32 v23, -v25, v23, v22
	v_cmp_lt_f32_e64 s[4:5], 0, v23
	s_nop 1
	v_cndmask_b32_e64 v23, v24, v25, s[4:5]
	v_mul_f32_e32 v24, 0x37800000, v23
	v_cndmask_b32_e32 v23, v23, v24, vcc
	v_cmp_class_f32_e32 vcc, v22, v222
	s_nop 1
	v_cndmask_b32_e32 v22, v23, v22, vcc
	v_div_scale_f32 v23, s[4:5], v22, v22, 1.0
	v_rcp_f32_e32 v24, v23
	s_add_u32 s4, s21, s14
	s_addc_u32 s5, s26, 0
	s_nop 1
	global_store_dwordx2 v0, v[2:3], s[4:5] offset:2048
	v_fma_f32 v2, -v23, v24, 1.0
	v_fmac_f32_e32 v24, v2, v24
	v_div_scale_f32 v2, vcc, 1.0, v22, 1.0
	v_mul_f32_e32 v3, v2, v24
	v_fma_f32 v25, -v23, v3, v2
	v_fmac_f32_e32 v3, v25, v24
	v_fma_f32 v2, -v23, v3, v2
	v_div_fmas_f32 v2, v2, v24, v3
	v_div_fixup_f32 v2, v2, v22, 1.0
	s_waitcnt vmcnt(7)
	v_lshlrev_b32_e32 v22, 16, v46
	v_and_b32_e32 v24, 0xffff0000, v46
	v_mul_f32_e32 v3, 0xbfb8aa3b, v22
	v_exp_f32_e32 v3, v3
	v_mul_f32_e32 v25, 0xbfb8aa3b, v24
	v_exp_f32_e32 v27, v25
	v_lshlrev_b32_e32 v23, 16, v47
	v_add_f32_e32 v3, 1.0, v3
	v_rcp_f32_e32 v26, v3
	v_add_f32_e32 v3, 1.0, v27
	v_rcp_f32_e32 v28, v3
	v_mul_f32_e32 v3, 0xbfb8aa3b, v23
	v_exp_f32_e32 v3, v3
	v_and_b32_e32 v25, 0xffff0000, v47
	s_mul_hi_u32 s4, s24, 0x1800
	s_add_i32 s4, s4, s25
	v_pk_mul_f32 v[30:31], v[30:31], v[2:3] op_sel_hi:[1,0]
	v_add_f32_e32 v3, 1.0, v3
	v_rcp_f32_e32 v27, v3
	v_mul_f32_e32 v3, 0xbfb8aa3b, v25
	v_exp_f32_e32 v3, v3
	v_pk_mul_f32 v[30:31], v[44:45], v[30:31]
	v_pk_mul_f32 v[22:23], v[26:27], v[22:23]
	s_mulk_i32 s24, 0x1800
	v_add_f32_e32 v3, 1.0, v3
	v_rcp_f32_e32 v29, v3
	v_pk_mul_f32 v[2:3], v[20:21], v[2:3] op_sel_hi:[1,0]
	v_pk_mul_f32 v[22:23], v[22:23], v[30:31]
	v_pk_mul_f32 v[2:3], v[4:5], v[2:3]
	v_pk_mul_f32 v[18:19], v[28:29], v[24:25]
	s_add_u32 s21, s0, s24
	v_pk_mul_f32 v[2:3], v[18:19], v[2:3]
	v_and_b32_sdwa v18, v23, v224 dst_sel:DWORD dst_unused:UNUSED_PAD src0_sel:WORD_1 src1_sel:DWORD
	v_and_b32_sdwa v20, v3, v224 dst_sel:DWORD dst_unused:UNUSED_PAD src0_sel:WORD_1 src1_sel:DWORD
	v_and_b32_sdwa v21, v2, v224 dst_sel:DWORD dst_unused:UNUSED_PAD src0_sel:WORD_1 src1_sel:DWORD
	v_add3_u32 v3, v3, v20, s40
	v_and_b32_sdwa v19, v22, v224 dst_sel:DWORD dst_unused:UNUSED_PAD src0_sel:WORD_1 src1_sel:DWORD
	v_add3_u32 v18, v23, v18, s40
	v_add3_u32 v2, v2, v21, s40
	v_and_b32_e32 v3, 0xffff0000, v3
	v_add3_u32 v19, v22, v19, s40
	v_and_b32_e32 v2, 0xffff0000, v2
	v_or_b32_sdwa v3, v3, v18 dst_sel:DWORD dst_unused:UNUSED_PAD src0_sel:DWORD src1_sel:WORD_1
	v_fmamk_f32 v18, v56, 0x3b800000, v225
	v_or_b32_sdwa v2, v2, v19 dst_sel:DWORD dst_unused:UNUSED_PAD src0_sel:DWORD src1_sel:WORD_1
	v_mul_f32_e32 v19, 0x4f800000, v18
	v_cmp_gt_f32_e32 vcc, s38, v18
	s_addc_u32 s24, s1, s4
	v_mov_b32_e32 v26, v14
	v_cndmask_b32_e32 v18, v18, v19, vcc
	v_sqrt_f32_e32 v19, v18
	v_mov_b32_e32 v27, v16
	v_mov_b32_e32 v16, v15
	v_add_u32_e32 v20, -1, v19
	v_fma_f32 v21, -v20, v19, v18
	v_cmp_ge_f32_e64 s[4:5], 0, v21
	v_add_u32_e32 v21, 1, v19
	s_nop 0
	v_cndmask_b32_e64 v20, v19, v20, s[4:5]
	v_fma_f32 v19, -v21, v19, v18
	v_cmp_lt_f32_e64 s[4:5], 0, v19
	s_nop 1
	v_cndmask_b32_e64 v19, v20, v21, s[4:5]
	v_mul_f32_e32 v20, 0x37800000, v19
	v_cndmask_b32_e32 v19, v19, v20, vcc
	v_cmp_class_f32_e32 vcc, v18, v222
	s_nop 1
	v_cndmask_b32_e32 v18, v19, v18, vcc
	v_div_scale_f32 v19, s[4:5], v18, v18, 1.0
	v_rcp_f32_e32 v20, v19
	s_add_u32 s4, s21, s14
	s_addc_u32 s5, s24, 0
	s_nop 1
	global_store_dwordx2 v0, v[2:3], s[4:5] offset:2048
	v_fma_f32 v2, -v19, v20, 1.0
	v_fmac_f32_e32 v20, v2, v20
	v_div_scale_f32 v2, vcc, 1.0, v18, 1.0
	v_mul_f32_e32 v3, v2, v20
	v_fma_f32 v21, -v19, v3, v2
	v_fmac_f32_e32 v3, v21, v20
	v_fma_f32 v2, -v19, v3, v2
	v_div_fmas_f32 v2, v2, v20, v3
	v_div_fixup_f32 v2, v2, v18, 1.0
	s_waitcnt vmcnt(7)
; __device__ __forceinline__ unsigned pk2(float lo, float hi) { return f2bf(lo) | (f2bf(hi) << 16); }
; __device__ __forceinline__ float bflo(unsigned w) { return __uint_as_float(w << 16); }
; __device__ __forceinline__ float bfhi(unsigned w) { return __uint_as_float(w & 0xffff0000u); }
; __device__ __forceinline__ void gla_g3(LAS unsigned char* lds, const bf16* Z, const bf16* ST, bf16* Oabc, const GlaPre pre, const float (&wa)[16], const float ba, const float* gla_norm, int item, int tid) {
;     ...
;       for (int j = 0; j < 8; ++j) { const int t = wid + NWAVES * j; const float rstd = 1.0f / sqrtf(ss[j] * (1.f / 256.f) + EPS);
;           const float r0 = bflo(rw[j].x), r1 = bfhi(rw[j].x), r2 = bflo(rw[j].y), r3 = bfhi(rw[j].y);
;           v2u w; w.x = pk2(ov[j].x * rstd * gn.x * (r0 * __builtin_amdgcn_rcpf(1.0f + __expf(-r0))), ov[j].y * rstd * gn.y * (r1 * __builtin_amdgcn_rcpf(1.0f + __expf(-r1))));
;           w.y = pk2(ov[j].z * rstd * gn.z * (r2 * __builtin_amdgcn_rcpf(1.0f + __expf(-r2))), ov[j].w * rstd * gn.w * (r3 * __builtin_amdgcn_rcpf(1.0f + __expf(-r3))));
;           *(v2u*)(Oabc + (m0 + t) * 3072 + 1024 + h * 256 + 4 * lane) = w; } }
	v_lshlrev_b32_e32 v18, 16, v42
	v_and_b32_e32 v20, 0xffff0000, v42
	v_mul_f32_e32 v3, 0xbfb8aa3b, v18
	v_exp_f32_e32 v3, v3
	v_mul_f32_e32 v21, 0xbfb8aa3b, v20
	v_exp_f32_e32 v23, v21
	v_lshlrev_b32_e32 v19, 16, v43
	v_add_f32_e32 v3, 1.0, v3
	v_rcp_f32_e32 v22, v3
	v_add_f32_e32 v3, 1.0, v23
	v_rcp_f32_e32 v24, v3
	v_mul_f32_e32 v3, 0xbfb8aa3b, v19
	v_exp_f32_e32 v3, v3
	v_and_b32_e32 v21, 0xffff0000, v43
	s_mul_hi_u32 s4, s22, 0x1800
	s_add_i32 s4, s4, s23
	v_pk_mul_f32 v[26:27], v[26:27], v[2:3] op_sel_hi:[1,0]
	v_add_f32_e32 v3, 1.0, v3
	v_rcp_f32_e32 v23, v3
	v_mul_f32_e32 v3, 0xbfb8aa3b, v21
	v_exp_f32_e32 v3, v3
	v_pk_mul_f32 v[26:27], v[44:45], v[26:27]
	v_pk_mul_f32 v[18:19], v[22:23], v[18:19]
	s_mulk_i32 s22, 0x1800
	v_add_f32_e32 v3, 1.0, v3
	v_rcp_f32_e32 v25, v3
	v_pk_mul_f32 v[2:3], v[16:17], v[2:3] op_sel_hi:[1,0]
	v_pk_mul_f32 v[18:19], v[18:19], v[26:27]
	v_pk_mul_f32 v[2:3], v[4:5], v[2:3]
	v_pk_mul_f32 v[14:15], v[24:25], v[20:21]
	s_add_u32 s21, s0, s22
	v_pk_mul_f32 v[2:3], v[14:15], v[2:3]
	v_and_b32_sdwa v14, v19, v224 dst_sel:DWORD dst_unused:UNUSED_PAD src0_sel:WORD_1 src1_sel:DWORD
	v_and_b32_sdwa v16, v3, v224 dst_sel:DWORD dst_unused:UNUSED_PAD src0_sel:WORD_1 src1_sel:DWORD
	v_and_b32_sdwa v17, v2, v224 dst_sel:DWORD dst_unused:UNUSED_PAD src0_sel:WORD_1 src1_sel:DWORD
	v_add3_u32 v3, v3, v16, s40
	v_and_b32_sdwa v15, v18, v224 dst_sel:DWORD dst_unused:UNUSED_PAD src0_sel:WORD_1 src1_sel:DWORD
	v_add3_u32 v14, v19, v14, s40
	v_add3_u32 v2, v2, v17, s40
	v_and_b32_e32 v3, 0xffff0000, v3
	v_add3_u32 v15, v18, v15, s40
	v_and_b32_e32 v2, 0xffff0000, v2
	v_or_b32_sdwa v3, v3, v14 dst_sel:DWORD dst_unused:UNUSED_PAD src0_sel:DWORD src1_sel:WORD_1
	v_fmamk_f32 v14, v55, 0x3b800000, v225
	v_or_b32_sdwa v2, v2, v15 dst_sel:DWORD dst_unused:UNUSED_PAD src0_sel:DWORD src1_sel:WORD_1
	v_mul_f32_e32 v15, 0x4f800000, v14
	v_cmp_gt_f32_e32 vcc, s38, v14
	s_addc_u32 s22, s1, s4
	v_mov_b32_e32 v22, v10
	v_cndmask_b32_e32 v14, v14, v15, vcc
	v_sqrt_f32_e32 v15, v14
	v_mov_b32_e32 v23, v12
	v_mov_b32_e32 v12, v11
	v_add_u32_e32 v16, -1, v15
	v_fma_f32 v17, -v16, v15, v14
	v_cmp_ge_f32_e64 s[4:5], 0, v17
	v_add_u32_e32 v17, 1, v15
	s_nop 0
	v_cndmask_b32_e64 v16, v15, v16, s[4:5]
	v_fma_f32 v15, -v17, v15, v14
	v_cmp_lt_f32_e64 s[4:5], 0, v15
	s_nop 1
	v_cndmask_b32_e64 v15, v16, v17, s[4:5]
	v_mul_f32_e32 v16, 0x37800000, v15
	v_cndmask_b32_e32 v15, v15, v16, vcc
	v_cmp_class_f32_e32 vcc, v14, v222
	s_nop 1
	v_cndmask_b32_e32 v14, v15, v14, vcc
	v_div_scale_f32 v15, s[4:5], v14, v14, 1.0
	v_rcp_f32_e32 v16, v15
	s_add_u32 s4, s21, s14
	s_addc_u32 s5, s22, 0
	s_nop 1
	global_store_dwordx2 v0, v[2:3], s[4:5] offset:2048
	v_fma_f32 v2, -v15, v16, 1.0
	v_fmac_f32_e32 v16, v2, v16
	v_div_scale_f32 v2, vcc, 1.0, v14, 1.0
	v_mul_f32_e32 v3, v2, v16
	v_fma_f32 v17, -v15, v3, v2
	v_fmac_f32_e32 v3, v17, v16
	v_fma_f32 v2, -v15, v3, v2
	v_div_fmas_f32 v2, v2, v16, v3
	v_div_fixup_f32 v2, v2, v14, 1.0
	s_waitcnt vmcnt(7)
; __device__ __forceinline__ unsigned pk2(float lo, float hi) { return f2bf(lo) | (f2bf(hi) << 16); }
; __device__ __forceinline__ float bflo(unsigned w) { return __uint_as_float(w << 16); }
; __device__ __forceinline__ float bfhi(unsigned w) { return __uint_as_float(w & 0xffff0000u); }
; #define INP(k) ldptr(PTAB, (k))
; __device__ __forceinline__ void gla_g3(LAS unsigned char* lds, const bf16* Z, const bf16* ST, bf16* Oabc, const GlaPre pre, const float (&wa)[16], const float ba, const float* gla_norm, int item, int tid) {
;     ...
;       for (int j = 0; j < 8; ++j) { const int t = wid + NWAVES * j; const float rstd = 1.0f / sqrtf(ss[j] * (1.f / 256.f) + EPS);
;           const float r0 = bflo(rw[j].x), r1 = bfhi(rw[j].x), r2 = bflo(rw[j].y), r3 = bfhi(rw[j].y);
;           v2u w; w.x = pk2(ov[j].x * rstd * gn.x * (r0 * __builtin_amdgcn_rcpf(1.0f + __expf(-r0))), ov[j].y * rstd * gn.y * (r1 * __builtin_amdgcn_rcpf(1.0f + __expf(-r1))));
;           w.y = pk2(ov[j].z * rstd * gn.z * (r2 * __builtin_amdgcn_rcpf(1.0f + __expf(-r2))), ov[j].w * rstd * gn.w * (r3 * __builtin_amdgcn_rcpf(1.0f + __expf(-r3))));
;           *(v2u*)(Oabc + (m0 + t) * 3072 + 1024 + h * 256 + 4 * lane) = w; } }
;     __syncthreads();
; __global__ void __launch_bounds__(NWAVES * 64, 2) fwd_kernel(Args args) {
;     ...
;               for (int it = vcu; it < 1024; it += G) { float wa[16], ba; gla_alpha_load(wa, ba, INP(6) + (size_t)l * 16 * 512, INP(7) + l * 512, (it >> 6) & 3, tid);
;                   const GlaPre cur = gla_blr_load(WSP(WS_ZABC), (size_t)(it >> 8) * SEQ + 64 * (it & 63), tid);
;                   gla_g3(ring, WSP(WS_ZABC), ((bf16*)xo), WSP(WS_OABC), cur, wa, ba, INP(8) + l * 1024, it, tid); } }
	v_lshlrev_b32_e32 v14, 16, v40
	v_and_b32_e32 v16, 0xffff0000, v40
	v_mul_f32_e32 v3, 0xbfb8aa3b, v14
	v_exp_f32_e32 v3, v3
	v_mul_f32_e32 v17, 0xbfb8aa3b, v16
	v_exp_f32_e32 v19, v17
	v_lshlrev_b32_e32 v15, 16, v41
	v_add_f32_e32 v3, 1.0, v3
	v_rcp_f32_e32 v18, v3
	v_add_f32_e32 v3, 1.0, v19
	v_rcp_f32_e32 v20, v3
	v_mul_f32_e32 v3, 0xbfb8aa3b, v15
	v_exp_f32_e32 v3, v3
	v_and_b32_e32 v17, 0xffff0000, v41
	s_mul_hi_u32 s4, s19, 0x1800
	s_add_i32 s4, s4, s20
	v_pk_mul_f32 v[22:23], v[22:23], v[2:3] op_sel_hi:[1,0]
	v_add_f32_e32 v3, 1.0, v3
	v_rcp_f32_e32 v19, v3
	v_mul_f32_e32 v3, 0xbfb8aa3b, v17
	v_exp_f32_e32 v3, v3
	v_pk_mul_f32 v[22:23], v[44:45], v[22:23]
	v_pk_mul_f32 v[14:15], v[18:19], v[14:15]
	s_mulk_i32 s19, 0x1800
	v_add_f32_e32 v3, 1.0, v3
	v_rcp_f32_e32 v21, v3
	v_pk_mul_f32 v[2:3], v[12:13], v[2:3] op_sel_hi:[1,0]
	v_pk_mul_f32 v[14:15], v[14:15], v[22:23]
	v_pk_mul_f32 v[2:3], v[4:5], v[2:3]
	v_pk_mul_f32 v[10:11], v[20:21], v[16:17]
	s_add_u32 s19, s0, s19
	v_pk_mul_f32 v[2:3], v[10:11], v[2:3]
	v_and_b32_sdwa v10, v15, v224 dst_sel:DWORD dst_unused:UNUSED_PAD src0_sel:WORD_1 src1_sel:DWORD
	v_and_b32_sdwa v12, v3, v224 dst_sel:DWORD dst_unused:UNUSED_PAD src0_sel:WORD_1 src1_sel:DWORD
	v_and_b32_sdwa v13, v2, v224 dst_sel:DWORD dst_unused:UNUSED_PAD src0_sel:WORD_1 src1_sel:DWORD
	v_add3_u32 v3, v3, v12, s40
	v_and_b32_sdwa v11, v14, v224 dst_sel:DWORD dst_unused:UNUSED_PAD src0_sel:WORD_1 src1_sel:DWORD
	v_add3_u32 v10, v15, v10, s40
	v_add3_u32 v2, v2, v13, s40
	v_and_b32_e32 v3, 0xffff0000, v3
	v_add3_u32 v11, v14, v11, s40
	v_and_b32_e32 v2, 0xffff0000, v2
	v_or_b32_sdwa v3, v3, v10 dst_sel:DWORD dst_unused:UNUSED_PAD src0_sel:DWORD src1_sel:WORD_1
	v_fmamk_f32 v10, v54, 0x3b800000, v225
	v_or_b32_sdwa v2, v2, v11 dst_sel:DWORD dst_unused:UNUSED_PAD src0_sel:DWORD src1_sel:WORD_1
	v_mul_f32_e32 v11, 0x4f800000, v10
	v_cmp_gt_f32_e32 vcc, s38, v10
	s_addc_u32 s20, s1, s4
	v_mov_b32_e32 v18, v6
	v_cndmask_b32_e32 v10, v10, v11, vcc
	v_sqrt_f32_e32 v11, v10
	v_mov_b32_e32 v19, v8
	v_mov_b32_e32 v8, v7
	v_add_u32_e32 v12, -1, v11
	v_fma_f32 v13, -v12, v11, v10
	v_cmp_ge_f32_e64 s[4:5], 0, v13
	v_add_u32_e32 v13, 1, v11
	s_nop 0
	v_cndmask_b32_e64 v12, v11, v12, s[4:5]
	v_fma_f32 v11, -v13, v11, v10
	v_cmp_lt_f32_e64 s[4:5], 0, v11
	s_nop 1
	v_cndmask_b32_e64 v11, v12, v13, s[4:5]
	v_mul_f32_e32 v12, 0x37800000, v11
	v_cndmask_b32_e32 v11, v11, v12, vcc
	v_cmp_class_f32_e32 vcc, v10, v222
	s_nop 1
	v_cndmask_b32_e32 v10, v11, v10, vcc
	v_div_scale_f32 v11, s[4:5], v10, v10, 1.0
	v_rcp_f32_e32 v12, v11
	s_add_u32 s4, s19, s14
	s_addc_u32 s5, s20, 0
	s_nop 1
	global_store_dwordx2 v0, v[2:3], s[4:5] offset:2048
	v_fma_f32 v2, -v11, v12, 1.0
	v_fmac_f32_e32 v12, v2, v12
	v_div_scale_f32 v2, vcc, 1.0, v10, 1.0
	v_mul_f32_e32 v3, v2, v12
	v_fma_f32 v13, -v11, v3, v2
	v_fmac_f32_e32 v3, v13, v12
	v_fma_f32 v2, -v11, v3, v2
	v_div_fmas_f32 v2, v2, v12, v3
	v_div_fixup_f32 v2, v2, v10, 1.0
	s_waitcnt vmcnt(7)
	v_lshlrev_b32_e32 v10, 16, v38
	v_and_b32_e32 v12, 0xffff0000, v38
	v_mul_f32_e32 v3, 0xbfb8aa3b, v10
	v_exp_f32_e32 v3, v3
	v_mul_f32_e32 v13, 0xbfb8aa3b, v12
	v_exp_f32_e32 v15, v13
	v_lshlrev_b32_e32 v11, 16, v39
	v_add_f32_e32 v3, 1.0, v3
	v_rcp_f32_e32 v14, v3
	v_add_f32_e32 v3, 1.0, v15
	v_rcp_f32_e32 v16, v3
	v_mul_f32_e32 v3, 0xbfb8aa3b, v11
	v_exp_f32_e32 v3, v3
	v_and_b32_e32 v13, 0xffff0000, v39
	s_mul_hi_u32 s4, s15, 0x1800
	s_add_i32 s4, s4, s18
	v_pk_mul_f32 v[18:19], v[18:19], v[2:3] op_sel_hi:[1,0]
	v_add_f32_e32 v3, 1.0, v3
	v_rcp_f32_e32 v15, v3
	v_mul_f32_e32 v3, 0xbfb8aa3b, v13
	v_exp_f32_e32 v3, v3
	v_pk_mul_f32 v[18:19], v[44:45], v[18:19]
	v_pk_mul_f32 v[10:11], v[14:15], v[10:11]
	s_mulk_i32 s15, 0x1800
	v_add_f32_e32 v3, 1.0, v3
	v_rcp_f32_e32 v17, v3
	v_pk_mul_f32 v[2:3], v[8:9], v[2:3] op_sel_hi:[1,0]
	v_pk_mul_f32 v[10:11], v[10:11], v[18:19]
	v_pk_mul_f32 v[2:3], v[4:5], v[2:3]
	v_pk_mul_f32 v[4:5], v[16:17], v[12:13]
	s_add_u32 s5, s0, s15
	v_pk_mul_f32 v[2:3], v[4:5], v[2:3]
	v_and_b32_sdwa v4, v11, v224 dst_sel:DWORD dst_unused:UNUSED_PAD src0_sel:WORD_1 src1_sel:DWORD
	v_and_b32_sdwa v6, v3, v224 dst_sel:DWORD dst_unused:UNUSED_PAD src0_sel:WORD_1 src1_sel:DWORD
	v_and_b32_sdwa v7, v2, v224 dst_sel:DWORD dst_unused:UNUSED_PAD src0_sel:WORD_1 src1_sel:DWORD
	v_and_b32_sdwa v5, v10, v224 dst_sel:DWORD dst_unused:UNUSED_PAD src0_sel:WORD_1 src1_sel:DWORD
	v_add3_u32 v3, v3, v6, s40
	v_add3_u32 v2, v2, v7, s40
	s_addc_u32 s15, s1, s4
	v_add3_u32 v5, v10, v5, s40
	v_add3_u32 v4, v11, v4, s40
	v_and_b32_e32 v3, 0xffff0000, v3
	v_and_b32_e32 v2, 0xffff0000, v2
	s_add_u32 s4, s5, s14
	v_or_b32_sdwa v3, v3, v4 dst_sel:DWORD dst_unused:UNUSED_PAD src0_sel:DWORD src1_sel:WORD_1
	v_or_b32_sdwa v2, v2, v5 dst_sel:DWORD dst_unused:UNUSED_PAD src0_sel:DWORD src1_sel:WORD_1
	s_addc_u32 s5, s15, 0
	global_store_dwordx2 v0, v[2:3], s[4:5] offset:2048
	v_readlane_b32 s4, v253, 59
	s_add_i32 s17, s17, s78
	s_add_i32 s16, s16, s4
	v_readlane_b32 s4, v254, 10
	v_readlane_b32 s5, v254, 11
	s_add_u32 s12, s12, s4
	s_addc_u32 s13, s13, s5
	s_cmpk_gt_i32 s17, 0x3ff
	s_barrier
	s_cbranch_scc1 .LBB0_1119
